# v18: v16 + GLA-C units drawn from an atomic ticket counter (tail balancing after the NSA queue) instead of the static blockIdx stride
# baseline (speedup 1.0000x reference)
.LBB0_989:
	v_mov_b32_e32 v3, v0
	s_cmpk_gt_i32 s72, 0x7ff
	v_readfirstlane_b32 s3, v3
	s_cbranch_scc1 .LBB0_1035
	v_mov_b32_e32 v182, 0xc500
	v_mov_b32_e32 v183, 0
	v_lshl_add_u64 v[180:181], s[96:97], 0, v[182:183]
	v_mov_b32_e32 v182, 1
	v_mov_b32_e32 v184, 0x27f00
	v_cmp_eq_u32_e64 s[100:101], 0, v0
	s_nop 1
	s_and_saveexec_b64 s[98:99], s[100:101]
	global_atomic_add v183, v[180:181], v182, off sc0
	s_mov_b64 exec, s[98:99]
	s_add_u32 s86, s96, 0x3a370000
	s_addc_u32 s87, s97, 0
	s_add_u32 s0, s96, 0xc2078000
	v_writelane_b32 v254, s0, 60
	s_waitcnt vmcnt(23)
	v_and_b32_e32 v5, 63, v3
	v_readlane_b32 s8, v254, 27
	s_waitcnt vmcnt(22)
	v_lshlrev_b32_e32 v8, 4, v5
	v_readlane_b32 s22, v254, 41
	v_readlane_b32 s23, v254, 42
	s_waitcnt vmcnt(2)
	v_ashrrev_i32_e32 v72, 4, v3
	s_addc_u32 s0, s97, 0
	s_ashr_i32 s2, s3, 6
	v_lshrrev_b32_e32 v14, 1, v72
	v_and_b32_e32 v15, 3, v72
	global_load_dwordx4 v[34:37], v8, s[22:23]
	v_and_b32_e32 v1, 0x7f, v3
	s_waitcnt vmcnt(2)
	v_mov_b32_e32 v71, 0
	v_and_or_b32 v14, v14, 4, v15
	v_lshlrev_b32_e32 v15, 4, v3
	s_lshl_b32 s8, s2, 5
	v_and_b32_e32 v7, 31, v3
	v_bfe_u32 v9, v3, 5, 1
	v_lshlrev_b32_e32 v74, 1, v1
	v_mov_b32_e32 v75, v71
	v_lshlrev_b32_e32 v14, 6, v14
	v_and_b32_e32 v16, 48, v15
	s_and_b32 s8, s8, 32
	v_writelane_b32 v255, s0, 0
	v_lshl_add_u64 v[76:77], s[86:87], 0, v[74:75]
	v_add3_u32 v75, 0, v14, v16
	s_lshl_b32 s0, s2, 3
	v_or_b32_e32 v16, s8, v7
	v_lshlrev_b32_e32 v22, 2, v9
	v_readlane_b32 s9, v254, 28
	v_readlane_b32 s10, v254, 29
	v_readlane_b32 s11, v254, 30
	v_readlane_b32 s12, v254, 31
	v_readlane_b32 s13, v254, 32
	v_readlane_b32 s14, v254, 33
	v_readlane_b32 s15, v254, 34
	v_readlane_b32 s16, v254, 35
	v_readlane_b32 s17, v254, 36
	v_readlane_b32 s18, v254, 37
	v_readlane_b32 s19, v254, 38
	v_readlane_b32 s20, v254, 39
	v_readlane_b32 s21, v254, 40
	v_writelane_b32 v254, s0, 61
	v_cmp_gt_u32_e64 s[0:1], v22, v16
	v_or_b32_e32 v46, 32, v22
	s_ashr_i32 s4, s3, 8
	v_writelane_b32 v254, s0, 62
	s_lshr_b32 s3, s3, 6
	v_lshlrev_b32_e32 v18, 4, v9
	v_writelane_b32 v254, s1, 63
	v_cmp_gt_u32_e64 s[0:1], v46, v16
	v_or_b32_e32 v46, 33, v22
	s_movk_i32 s9, 0x70
	v_writelane_b32 v255, s0, 20
	v_lshlrev_b32_e32 v2, 2, v5
	v_lshl_add_u32 v10, v7, 2, 0
	v_writelane_b32 v255, s1, 21
	v_cmp_lt_u32_e64 s[0:1], v22, v16
	s_and_b32 s3, s3, 2
	v_and_b32_e32 v19, 0x70, v15
	v_writelane_b32 v255, s0, 10
	s_movk_i32 s11, 0xfc
	v_bitop3_b32 v15, v18, v15, s9 bitop3:0x78
	v_writelane_b32 v255, s1, 11
	v_cmp_gt_u32_e64 s[0:1], v46, v16
	v_or_b32_e32 v46, 2, v22
	s_movk_i32 s9, 0x60
	v_writelane_b32 v255, s0, 24
	v_lshlrev_b32_e32 v5, 3, v5
	v_and_b32_e32 v9, 0xc0, v8
	v_writelane_b32 v255, s1, 25
	v_cmp_gt_u32_e64 s[0:1], v46, v16
	v_or_b32_e32 v46, 34, v22
	v_lshlrev_b32_e32 v23, 1, v3
	v_writelane_b32 v255, s0, 14
	v_mad_u32_u24 v7, v7, s11, v10
	v_bitop3_b32 v20, v18, v19, 32 bitop3:0x36
	v_writelane_b32 v255, s1, 15
	v_cmp_gt_u32_e64 s[0:1], v46, v16
	v_or_b32_e32 v46, 3, v22
	v_bitop3_b32 v21, v18, v19, 64 bitop3:0x36
	v_writelane_b32 v255, s0, 16
	v_bitop3_b32 v19, v18, v19, s9 bitop3:0x36
	v_and_or_b32 v9, v5, 24, v9
	v_writelane_b32 v255, s1, 17
	v_cmp_gt_u32_e64 s[0:1], v46, v16
	v_or_b32_e32 v46, 35, v22
	v_and_b32_e32 v23, 32, v23
	v_writelane_b32 v255, s0, 26
	v_and_b32_e32 v5, 0x100, v5
	s_lshl_b32 s9, s3, 9
	v_writelane_b32 v255, s1, 27
	v_cmp_gt_u32_e64 s[0:1], v46, v16
	v_or_b32_e32 v46, 8, v22
	s_lshl_b32 s11, s4, 14
	v_writelane_b32 v255, s0, 22
	s_add_i32 s12, 0, 0xa000
	v_add3_u32 v5, v5, s12, v23
	v_writelane_b32 v255, s1, 23
	v_cmp_gt_u32_e64 s[0:1], v46, v16
	v_or_b32_e32 v46, 40, v22
	s_or_b32 s9, s9, s11
	v_writelane_b32 v254, s0, 58
	s_movk_i32 s33, 0x2e00
	v_add3_u32 v113, s9, v5, v9
	v_writelane_b32 v254, s1, 59
	v_cmp_gt_u32_e64 s[0:1], v46, v16
	v_or_b32_e32 v46, 9, v22
	v_or_b32_e32 v5, s8, v22
	v_writelane_b32 v255, s0, 6
	v_ashrrev_i32_e32 v73, 31, v72
	v_mad_i64_i32 v[78:79], s[8:9], v72, s33, 0
	v_writelane_b32 v255, s1, 7
	v_cmp_gt_u32_e64 s[0:1], v46, v16
	v_or_b32_e32 v46, 41, v22
	v_add_u32_e32 v23, 0, v8
	v_writelane_b32 v255, s0, 8
	v_lshlrev_b64 v[80:81], 9, v[72:73]
	s_mov_b64 s[8:9], 0x8000
	v_writelane_b32 v255, s1, 9
	v_cmp_gt_u32_e64 s[0:1], v46, v16
	v_or_b32_e32 v46, 10, v22
	v_add_u32_e32 v8, 32, v72
	v_writelane_b32 v255, s0, 2
	v_lshl_add_u64 v[82:83], v[80:81], 0, s[8:9]
	v_mad_i64_i32 v[84:85], s[8:9], v8, s33, 0
	v_writelane_b32 v255, s1, 3
	v_cmp_gt_u32_e64 s[0:1], v46, v16
	v_or_b32_e32 v46, 42, v22
	v_lshlrev_b32_e32 v13, 1, v72
	v_writelane_b32 v255, s0, 4
	s_mov_b64 s[8:9], 0xc000
	v_lshlrev_b32_e32 v11, 3, v3
	v_writelane_b32 v255, s1, 5
	v_cmp_gt_u32_e64 s[0:1], v46, v16
	v_or_b32_e32 v46, 11, v22
	v_cmp_gt_u32_e64 s[38:39], v46, v16
	v_or_b32_e32 v46, 43, v22
	v_cmp_gt_u32_e64 s[40:41], v46, v16
	v_or_b32_e32 v46, 16, v22
	v_cmp_gt_u32_e64 s[42:43], v46, v16
	v_or_b32_e32 v46, 48, v22
	v_cmp_gt_u32_e64 s[44:45], v46, v16
	v_or_b32_e32 v46, 17, v22
	v_cmp_gt_u32_e64 s[46:47], v46, v16
	v_or_b32_e32 v46, 49, v22
	v_cmp_gt_u32_e64 s[48:49], v46, v16
	v_or_b32_e32 v46, 18, v22
	v_cmp_gt_u32_e64 s[50:51], v46, v16
	v_or_b32_e32 v46, 50, v22
	v_cmp_gt_u32_e64 s[52:53], v46, v16
	v_or_b32_e32 v46, 19, v22
	v_and_b32_e32 v6, 15, v3
	v_ashrrev_i32_e32 v12, 3, v3
	v_and_b32_e32 v13, 8, v13
	v_lshl_add_u32 v112, v3, 2, 0
	v_and_b32_e32 v14, 1, v3
	v_lshl_add_u64 v[88:89], v[80:81], 0, s[8:9]
	v_add_u32_e32 v3, 0x200, v3
	s_mov_b32 s8, 0xfffff0
	v_cmp_gt_u32_e64 s[54:55], v46, v16
	v_or_b32_e32 v46, 51, v22
	v_ashrrev_i32_e32 v73, 4, v3
	v_and_or_b32 v3, v72, s8, v13
	v_cmp_gt_u32_e64 s[56:57], v46, v16
	v_or_b32_e32 v46, 24, v22
	v_and_b32_e32 v4, 0x78, v11
	v_bfe_u32 v11, v11, 5, 2
	v_lshrrev_b32_e32 v3, 1, v3
	v_cmp_gt_u32_e64 s[58:59], v46, v16
	v_or_b32_e32 v46, 56, v22
	v_or_b32_e32 v3, v3, v11
	v_cmp_gt_u32_e64 s[60:61], v46, v16
	v_or_b32_e32 v46, 25, v22
	v_lshlrev_b32_e32 v116, 9, v3
	v_and_or_b32 v3, v8, s8, v13
	v_cmp_gt_u32_e64 s[62:63], v46, v16
	v_or_b32_e32 v46, 57, v22
	v_and_b32_e32 v110, -16, v12
	s_lshl_b32 s4, s4, 9
	v_lshrrev_b32_e32 v3, 1, v3
	v_cmp_gt_u32_e64 s[64:65], v46, v16
	v_or_b32_e32 v46, 26, v22
	v_mul_u32_u24_e32 v5, 0x410, v5
	s_movk_i32 s10, 0x110
	v_ashrrev_i32_e32 v9, 31, v8
	v_or_b32_e32 v3, v3, v11
	v_lshl_add_u32 v120, v110, 8, 0
	v_or_b32_e32 v12, 15, v12
	v_writelane_b32 v255, s0, 12
	v_cmp_gt_u32_e64 s[66:67], v46, v16
	v_or_b32_e32 v46, 58, v22
	v_add3_u32 v121, v10, s4, v5
	v_cmp_eq_u32_e64 s[76:77], 0, v14
	v_add_u32_e32 v14, 0, v74
	v_mad_u32_u24 v17, v16, s10, 0
	v_lshlrev_b64 v[86:87], 9, v[8:9]
	v_lshlrev_b32_e32 v117, 9, v3
	v_mul_lo_u32 v3, v110, s10
	v_add_u32_e32 v8, 0x100, v120
	v_xor_b32_e32 v9, 16, v74
	v_add_u32_e32 v11, 0x200, v120
	v_xor_b32_e32 v13, 32, v74
	v_add_u32_e32 v24, 0x300, v120
	v_xor_b32_e32 v25, 48, v74
	v_add_u32_e32 v26, 0x400, v120
	v_xor_b32_e32 v27, 64, v74
	v_add_u32_e32 v28, 0x500, v120
	v_xor_b32_e32 v29, 0x50, v74
	v_add_u32_e32 v30, 0x600, v120
	v_xor_b32_e32 v31, 0x60, v74
	v_add_u32_e32 v32, 0x700, v120
	v_xor_b32_e32 v33, 0x70, v74
	v_add_u32_e32 v38, 0x800, v120
	v_add_u32_e32 v39, 0x900, v120
	v_add_u32_e32 v40, 0xa00, v120
	v_add_u32_e32 v41, 0xb00, v120
	v_add_u32_e32 v42, 0xc00, v120
	v_add_u32_e32 v43, 0xd00, v120
	v_add_u32_e32 v44, 0xe00, v120
	v_mul_lo_u32 v45, v12, s10
	v_lshl_add_u32 v12, v12, 8, 0
	v_writelane_b32 v255, s1, 13
	s_mov_b32 s28, s72
	v_cmp_gt_u32_e64 s[68:69], v46, v16
	v_or_b32_e32 v46, 27, v22
	v_or_b32_e32 v22, 59, v22
	v_add_u32_e32 v5, 0xa000, v121
	s_lshl_b32 s27, s3, 7
	s_mulk_i32 s2, 0x2080
	v_readlane_b32 s0, v254, 53
	s_mov_b32 s35, 0
	v_add_u32_e32 v111, 0xa000, v75
	v_add_u32_e32 v114, 0x8000, v113
	v_add_u32_e32 v115, 0x10000, v113
	v_add_u32_e32 v118, 0x1a000, v75
	v_add_u32_e32 v119, 0x1e000, v75
	v_cmp_gt_u32_e64 s[70:71], v46, v16
	v_cmp_gt_u32_e64 s[72:73], v22, v16
	s_lshl_b32 s36, s28, 6
	s_lshl_b32 s37, s0, 6
	s_lshl_b32 s16, s28, 4
	s_lshl_b32 s17, s0, 4
	v_lshlrev_b32_e32 v70, 1, v4
	v_lshlrev_b32_e32 v90, 1, v6
	s_movk_i32 s18, 0x1000
	s_movk_i32 s19, 0x2000
	s_mov_b32 s20, 0xbfb8aa3b
	s_mov_b32 s21, 0x800000
	s_mov_b32 s22, 0x3f317217
	s_mov_b32 s23, 0x7f800000
	v_add_u32_e32 v122, v8, v9
	v_add_u32_e32 v123, v11, v13
	v_add_u32_e32 v124, v24, v25
	v_add_u32_e32 v125, v26, v27
	v_add_u32_e32 v126, v28, v29
	v_add_u32_e32 v127, v30, v31
	v_add_u32_e32 v128, v32, v33
	v_add_u32_e32 v129, v38, v74
	v_add_u32_e32 v130, v39, v9
	v_add_u32_e32 v131, v40, v13
	v_add_u32_e32 v132, v41, v25
	v_add_u32_e32 v133, v42, v27
	v_add_u32_e32 v134, v43, v29
	v_add_u32_e32 v135, v44, v31
	v_add_u32_e32 v136, v14, v45
	v_add_u32_e32 v137, v12, v33
	v_lshlrev_b32_e32 v92, 1, v2
	v_add_u32_e32 v138, v17, v18
	v_add_u32_e32 v139, v7, v15
	v_add_u32_e32 v140, v7, v20
	v_add_u32_e32 v141, v7, v21
	v_add_u32_e32 v142, v7, v19
	v_add_u32_e32 v143, s27, v5
	v_add_u32_e32 v144, s2, v23
	s_mov_b32 s26, 0x3b800000
	s_mov_b32 s24, 0x55d70000
	v_mov_b32_e32 v145, 0x41b17218
	v_add_u32_e32 v146, v14, v3
	s_waitcnt vmcnt(0)
	s_and_saveexec_b64 s[98:99], s[100:101]
	ds_write_b32 v184, v183
	s_mov_b64 exec, s[98:99]
	s_waitcnt lgkmcnt(0)
	s_barrier
	ds_read_b32 v185, v184
	s_waitcnt lgkmcnt(0)
	s_barrier
	v_readfirstlane_b32 s28, v185
	s_lshl_b32 s36, s28, 6
	s_lshl_b32 s16, s28, 4
	s_cmpk_gt_i32 s28, 0x7ff
	s_cbranch_scc1 .LBB0_1034
	s_branch .LBB0_992
.LBB0_991:
	s_or_b64 exec, exec, s[2:3]
	v_readlane_b32 s0, v254, 61
	s_add_i32 s74, s25, s0
	s_ashr_i32 s75, s74, 31
	s_mul_i32 s3, s74, 0x2e00
	s_mul_hi_i32 s2, s74, 0x2e00
	s_add_u32 s3, s86, s3
	s_addc_u32 s8, s87, s2
	s_lshl_b32 s4, s34, 1
	s_add_u32 s2, s3, s4
	s_addc_u32 s3, s8, 0
	v_mov_b32_e32 v93, v71
	v_lshl_add_u64 v[2:3], s[2:3], 0, v[92:93]
	v_add_co_u32_e32 v98, vcc, s19, v2
	s_waitcnt lgkmcnt(0)
	s_barrier
	v_addc_co_u32_e32 v99, vcc, 0, v3, vcc
	ds_read_b128 v[2:5], v139
	ds_read_b128 v[42:45], v138 offset:16384
	s_or_b32 s94, s74, 1
	s_ashr_i32 s95, s94, 31
	s_mul_i32 s3, s94, 0x2e00
	s_mul_hi_i32 s2, s94, 0x2e00
	s_add_u32 s3, s86, s3
	s_addc_u32 s8, s87, s2
	s_add_u32 s2, s3, s4
	ds_read_b128 v[46:49], v138 offset:16416
	ds_read_b128 v[18:21], v139 offset:8192
	ds_read_b128 v[50:53], v139 offset:128
	s_addc_u32 s3, s8, 0
	s_waitcnt lgkmcnt(3)
	v_mfma_f32_32x32x16_bf16 v[2:17], v[2:5], v[42:45], 0
	v_lshl_add_u64 v[22:23], s[2:3], 0, v[92:93]
	v_add_co_u32_e32 v100, vcc, s19, v22
	s_or_b32 s12, s74, 2
	s_nop 0
	v_addc_co_u32_e32 v101, vcc, 0, v23, vcc
	s_ashr_i32 s13, s12, 31
	s_waitcnt lgkmcnt(1)
	v_mfma_f32_32x32x16_bf16 v[18:33], v[18:21], v[42:45], 0
	ds_read_b128 v[38:41], v140
	ds_read_b128 v[54:57], v139 offset:8320
	s_mul_i32 s3, s12, 0x2e00
	s_mul_hi_i32 s2, s12, 0x2e00
	s_add_u32 s3, s86, s3
	s_addc_u32 s8, s87, s2
	s_add_u32 s2, s3, s4
	ds_read_b128 v[58:61], v140 offset:8192
	ds_read_b128 v[94:97], v140 offset:128
	s_addc_u32 s3, s8, 0
	s_waitcnt lgkmcnt(3)
	v_mfma_f32_32x32x16_bf16 v[2:17], v[38:41], v[46:49], v[2:17]
	v_lshl_add_u64 v[38:39], s[2:3], 0, v[92:93]
	v_add_co_u32_e32 v102, vcc, s19, v38
	s_or_b32 s10, s74, 3
	s_nop 0
	v_addc_co_u32_e32 v103, vcc, 0, v39, vcc
	ds_read_b128 v[38:41], v141
	ds_read_b128 v[148:151], v140 offset:8320
	s_waitcnt lgkmcnt(3)
	v_mfma_f32_32x32x16_bf16 v[18:33], v[58:61], v[46:49], v[18:33]
	ds_read_b128 v[62:65], v138 offset:16448
	ds_read_b128 v[66:69], v138 offset:16480
	ds_read_b128 v[58:61], v141 offset:8192
	ds_read_b128 v[152:155], v141 offset:128
	s_ashr_i32 s11, s10, 31
	s_mul_i32 s3, s10, 0x2e00
	s_mul_hi_i32 s2, s10, 0x2e00
	s_add_u32 s3, s86, s3
	s_addc_u32 s8, s87, s2
	s_waitcnt lgkmcnt(3)
	v_mfma_f32_32x32x16_bf16 v[2:17], v[38:41], v[62:65], v[2:17]
	s_add_u32 s2, s3, s4
	s_addc_u32 s3, s8, 0
	ds_read_b128 v[38:41], v142
	ds_read_b128 v[156:159], v141 offset:8320
	s_or_b32 s8, s74, 4
	s_ashr_i32 s9, s8, 31
	v_readlane_b32 s0, v254, 62
	v_readlane_b32 s1, v254, 63
	s_waitcnt lgkmcnt(3)
	v_mfma_f32_32x32x16_bf16 v[18:33], v[58:61], v[62:65], v[18:33]
	v_lshl_add_u64 v[58:59], s[2:3], 0, v[92:93]
	v_add_co_u32_e32 v164, vcc, s19, v58
	s_mul_i32 s3, s8, 0x2e00
	s_nop 0
	v_addc_co_u32_e32 v165, vcc, 0, v59, vcc
	ds_read_b128 v[58:61], v142 offset:8192
	ds_read_b128 v[160:163], v142 offset:128
	s_waitcnt lgkmcnt(3)
	v_mfma_f32_32x32x16_bf16 v[2:17], v[38:41], v[66:69], v[2:17]
	global_load_dwordx2 v[108:109], v[98:99], off offset:1024
	global_load_dwordx2 v[106:107], v[100:101], off offset:1024
	global_load_dwordx2 v[104:105], v[102:103], off offset:1024
	s_nop 0
	global_load_dwordx2 v[100:101], v[164:165], off offset:1024
	s_mul_hi_i32 s2, s8, 0x2e00
	s_add_u32 s3, s86, s3
	s_addc_u32 s25, s87, s2
	s_add_u32 s2, s3, s4
	s_addc_u32 s3, s25, 0
	s_or_b32 s92, s74, 5
	s_waitcnt lgkmcnt(1)
	v_mfma_f32_32x32x16_bf16 v[18:33], v[58:61], v[66:69], v[18:33]
	ds_read_b128 v[58:61], v138 offset:16512
	ds_read_b128 v[38:41], v138 offset:16544
	s_ashr_i32 s93, s92, 31
	ds_read_b128 v[164:167], v142 offset:8320
	s_waitcnt lgkmcnt(2)
	v_mfma_f32_32x32x16_bf16 v[2:17], v[50:53], v[58:61], v[2:17]
	v_lshl_add_u64 v[50:51], s[2:3], 0, v[92:93]
	s_mul_i32 s3, s92, 0x2e00
	s_mul_hi_i32 s2, s92, 0x2e00
	s_add_u32 s3, s86, s3
	s_addc_u32 s25, s87, s2
	s_add_u32 s2, s3, s4
	v_add_co_u32_e32 v98, vcc, s19, v50
	s_addc_u32 s3, s25, 0
	s_or_b32 s90, s74, 6
	v_addc_co_u32_e32 v99, vcc, 0, v51, vcc
	v_lshl_add_u64 v[50:51], s[2:3], 0, v[92:93]
	s_ashr_i32 s91, s90, 31
	s_mul_i32 s3, s90, 0x2e00
	s_mul_hi_i32 s2, s90, 0x2e00
	s_add_u32 s3, s86, s3
	s_addc_u32 s25, s87, s2
	s_add_u32 s2, s3, s4
	v_mfma_f32_32x32x16_bf16 v[18:33], v[54:57], v[58:61], v[18:33]
	s_addc_u32 s3, s25, 0
	ds_read_b128 v[54:57], v138 offset:16576
	s_waitcnt lgkmcnt(2)
	v_mfma_f32_32x32x16_bf16 v[2:17], v[94:97], v[38:41], v[2:17]
	v_add_co_u32_e32 v94, vcc, s19, v50
	v_lshl_add_u64 v[96:97], s[2:3], 0, v[92:93]
	s_or_b32 s2, s74, 7
	v_addc_co_u32_e32 v95, vcc, 0, v51, vcc
	s_ashr_i32 s3, s2, 31
	s_mul_i32 s29, s2, 0x2e00
	v_add_co_u32_e32 v96, vcc, s19, v96
	s_mul_hi_i32 s25, s2, 0x2e00
	s_add_u32 s29, s86, s29
	v_addc_co_u32_e32 v97, vcc, 0, v97, vcc
	s_addc_u32 s25, s87, s25
	s_add_u32 vcc_lo, s29, s4
	s_addc_u32 vcc_hi, s25, 0
	v_lshl_add_u64 v[102:103], vcc, 0, v[92:93]
	v_mfma_f32_32x32x16_bf16 v[18:33], v[148:151], v[38:41], v[18:33]
	v_add_co_u32_e32 v148, vcc, s19, v102
	ds_read_b128 v[50:53], v138 offset:16608
	s_nop 0
	v_addc_co_u32_e32 v149, vcc, 0, v103, vcc
	global_load_dwordx2 v[102:103], v[98:99], off offset:1024
	s_nop 0
	global_load_dwordx2 v[98:99], v[94:95], off offset:1024
	s_nop 0
	global_load_dwordx2 v[96:97], v[96:97], off offset:1024
	s_nop 0
	global_load_dwordx2 v[94:95], v[148:149], off offset:1024
	s_waitcnt lgkmcnt(1)
	v_mfma_f32_32x32x16_bf16 v[2:17], v[152:155], v[54:57], v[2:17]
	v_mfma_f32_32x32x16_bf16 v[18:33], v[156:159], v[54:57], v[18:33]
	s_waitcnt lgkmcnt(0)
	v_mfma_f32_32x32x16_bf16 v[2:17], v[160:163], v[50:53], v[2:17]
	v_mfma_f32_32x32x16_bf16 v[18:33], v[164:167], v[50:53], v[18:33]
	s_nop 10
	v_cndmask_b32_e64 v2, v2, 0, s[0:1]
	v_readlane_b32 s0, v255, 20
	v_readlane_b32 s1, v255, 21
	v_cndmask_b32_e64 v9, v9, 0, s[38:39]
	v_cndmask_b32_e64 v10, v10, 0, s[42:43]
	v_cndmask_b32_e64 v11, v11, 0, s[46:47]
	v_cndmask_b32_e64 v12, v12, 0, s[50:51]
	v_cndmask_b32_e64 v91, v18, 0, s[0:1]
	v_readlane_b32 s0, v255, 10
	v_readlane_b32 s1, v255, 11
	v_cndmask_b32_e64 v25, v25, 0, s[40:41]
	v_cndmask_b32_e64 v26, v26, 0, s[44:45]
	v_cndmask_b32_e64 v3, 0, v3, s[0:1]
	v_readlane_b32 s0, v255, 24
	v_readlane_b32 s1, v255, 25
	v_cndmask_b32_e64 v27, v27, 0, s[48:49]
	v_cndmask_b32_e64 v28, v28, 0, s[52:53]
	v_cndmask_b32_e64 v147, v19, 0, s[0:1]
	v_readlane_b32 s0, v255, 14
	v_readlane_b32 s1, v255, 15
	v_cndmask_b32_e64 v13, v13, 0, s[54:55]
	v_cndmask_b32_e64 v29, v29, 0, s[56:57]
	v_cndmask_b32_e64 v4, v4, 0, s[0:1]
	v_readlane_b32 s0, v255, 16
	v_readlane_b32 s1, v255, 17
	v_cndmask_b32_e64 v14, v14, 0, s[58:59]
	v_cndmask_b32_e64 v30, v30, 0, s[60:61]
	v_cndmask_b32_e64 v153, v20, 0, s[0:1]
	v_readlane_b32 s0, v255, 26
	v_readlane_b32 s1, v255, 27
	v_cndmask_b32_e64 v15, v15, 0, s[62:63]
	v_cndmask_b32_e64 v31, v31, 0, s[64:65]
	v_cndmask_b32_e64 v5, v5, 0, s[0:1]
	v_readlane_b32 s0, v255, 22
	v_readlane_b32 s1, v255, 23
	v_cndmask_b32_e64 v16, v16, 0, s[66:67]
	v_cndmask_b32_e64 v32, v32, 0, s[68:69]
	v_cndmask_b32_e64 v154, v21, 0, s[0:1]
	v_readlane_b32 s0, v254, 58
	v_readlane_b32 s1, v254, 59
	v_cndmask_b32_e64 v17, v17, 0, s[70:71]
	v_cndmask_b32_e64 v33, v33, 0, s[72:73]
	v_cndmask_b32_e64 v6, v6, 0, s[0:1]
	v_readlane_b32 s0, v255, 6
	v_readlane_b32 s1, v255, 7
	v_cvt_pk_bf16_f32 v18, v2, v3
	v_cvt_pk_bf16_f32 v19, v4, v5
	s_nop 1
	v_cndmask_b32_e64 v22, v22, 0, s[0:1]
	v_readlane_b32 s0, v255, 8
	v_readlane_b32 s1, v255, 9
	s_nop 1
	v_cndmask_b32_e64 v7, v7, 0, s[0:1]
	v_readlane_b32 s0, v255, 2
	v_readlane_b32 s1, v255, 3
	v_cvt_pk_bf16_f32 v20, v6, v7
	s_nop 0
	v_permlane32_swap_b32_e32 v18, v20
	v_cndmask_b32_e64 v23, v23, 0, s[0:1]
	v_readlane_b32 s0, v255, 4
	v_readlane_b32 s1, v255, 5
	s_nop 1
	v_cndmask_b32_e64 v8, v8, 0, s[0:1]
	v_readlane_b32 s0, v255, 12
	v_readlane_b32 s1, v255, 13
	v_cvt_pk_bf16_f32 v21, v8, v9
	v_cvt_pk_bf16_f32 v148, v10, v11
	v_cvt_pk_bf16_f32 v149, v12, v13
	v_cvt_pk_bf16_f32 v150, v14, v15
	v_cvt_pk_bf16_f32 v151, v16, v17
	s_nop 1
	v_cndmask_b32_e64 v24, v24, 0, s[0:1]
	v_cvt_pk_bf16_f32 v152, v91, v147
	v_cvt_pk_bf16_f32 v153, v153, v154
	v_cvt_pk_bf16_f32 v154, v22, v23
	v_cvt_pk_bf16_f32 v155, v24, v25
	v_cvt_pk_bf16_f32 v156, v26, v27
	v_cvt_pk_bf16_f32 v157, v28, v29
	v_cvt_pk_bf16_f32 v158, v30, v31
	v_cvt_pk_bf16_f32 v159, v32, v33
	ds_read_b64_tr_b16 v[2:3], v113 offset:0
	ds_read_b64_tr_b16 v[4:5], v113 offset:0x800
	ds_read_b64_tr_b16 v[22:23], v113 offset:0x1000
	ds_read_b64_tr_b16 v[24:25], v113 offset:0x1800
	ds_read_b64_tr_b16 v[26:27], v113 offset:0x2000
	ds_read_b64_tr_b16 v[28:29], v113 offset:0x2800
	ds_read_b64_tr_b16 v[30:31], v113 offset:0x3000
	ds_read_b64_tr_b16 v[32:33], v113 offset:0x3800
	ds_read_b64_tr_b16 v[160:161], v113 offset:0x200
	ds_read_b64_tr_b16 v[162:163], v113 offset:0xa00
	ds_read_b64_tr_b16 v[164:165], v113 offset:0x1200
	ds_read_b64_tr_b16 v[166:167], v113 offset:0x1a00
	ds_read_b64_tr_b16 v[168:169], v113 offset:0x2200
	ds_read_b64_tr_b16 v[170:171], v113 offset:0x2a00
	ds_read_b64_tr_b16 v[172:173], v113 offset:0x3200
	ds_read_b64_tr_b16 v[174:175], v113 offset:0x3a00
	s_nop 0
	s_waitcnt lgkmcnt(8)
	v_permlane32_swap_b32_e32 v19, v21
	v_permlane32_swap_b32_e32 v148, v150
	v_permlane32_swap_b32_e32 v149, v151
	v_permlane32_swap_b32_e32 v152, v154
	v_permlane32_swap_b32_e32 v153, v155
	v_permlane32_swap_b32_e32 v156, v158
	v_permlane32_swap_b32_e32 v157, v159
	v_mfma_f32_32x32x16_bf16 v[2:17], v[18:21], v[2:5], 0
	v_mfma_f32_32x32x16_bf16 v[2:17], v[148:151], v[22:25], v[2:17]
	v_mfma_f32_32x32x16_bf16 v[2:17], v[152:155], v[26:29], v[2:17]
	v_mfma_f32_32x32x16_bf16 v[2:17], v[156:159], v[30:33], v[2:17]
	s_waitcnt lgkmcnt(0)
	s_nop 0
	v_mfma_f32_32x32x16_bf16 v[18:33], v[18:21], v[160:163], 0
	v_mfma_f32_32x32x16_bf16 v[18:33], v[148:151], v[164:167], v[18:33]
	ds_read_b64_tr_b16 v[148:149], v114 offset:0
	ds_read_b64_tr_b16 v[150:151], v114 offset:0x800
	v_mfma_f32_32x32x16_bf16 v[18:33], v[152:155], v[168:171], v[18:33]
	ds_read_b64_tr_b16 v[152:153], v114 offset:0x1000
	ds_read_b64_tr_b16 v[154:155], v114 offset:0x1800
	v_mfma_f32_32x32x16_bf16 v[18:33], v[156:159], v[172:175], v[18:33]
	ds_read_b64_tr_b16 v[156:157], v114 offset:0x2000
	ds_read_b64_tr_b16 v[158:159], v114 offset:0x2800
	ds_read_b64_tr_b16 v[160:161], v114 offset:0x3000
	ds_read_b64_tr_b16 v[162:163], v114 offset:0x3800
	ds_read_b64_tr_b16 v[164:165], v114 offset:0x200
	ds_read_b64_tr_b16 v[166:167], v114 offset:0xa00
	ds_read_b64_tr_b16 v[168:169], v114 offset:0x1200
	ds_read_b64_tr_b16 v[170:171], v114 offset:0x1a00
	ds_read_b64_tr_b16 v[172:173], v114 offset:0x2200
	ds_read_b64_tr_b16 v[174:175], v114 offset:0x2a00
	ds_read_b64_tr_b16 v[176:177], v114 offset:0x3200
	ds_read_b64_tr_b16 v[178:179], v114 offset:0x3a00
	s_nop 0
	s_waitcnt lgkmcnt(8)
	s_nop 0
	v_mfma_f32_32x32x16_bf16 v[2:17], v[42:45], v[148:151], v[2:17]
	v_mfma_f32_32x32x16_bf16 v[2:17], v[46:49], v[152:155], v[2:17]
	v_mfma_f32_32x32x16_bf16 v[2:17], v[62:65], v[156:159], v[2:17]
	v_mfma_f32_32x32x16_bf16 v[2:17], v[66:69], v[160:163], v[2:17]
	s_waitcnt lgkmcnt(0)
	s_nop 0
	v_mfma_f32_32x32x16_bf16 v[18:33], v[42:45], v[164:167], v[18:33]
	ds_read_b64_tr_b16 v[42:43], v115 offset:0
	ds_read_b64_tr_b16 v[44:45], v115 offset:0x800
	v_mfma_f32_32x32x16_bf16 v[18:33], v[46:49], v[168:171], v[18:33]
	ds_read_b64_tr_b16 v[46:47], v115 offset:0x1000
	ds_read_b64_tr_b16 v[48:49], v115 offset:0x1800
	v_mfma_f32_32x32x16_bf16 v[18:33], v[62:65], v[172:175], v[18:33]
	ds_read_b64_tr_b16 v[62:63], v115 offset:0x2000
	ds_read_b64_tr_b16 v[64:65], v115 offset:0x2800
	v_mfma_f32_32x32x16_bf16 v[18:33], v[66:69], v[176:179], v[18:33]
	ds_read_b64_tr_b16 v[66:67], v115 offset:0x3000
	ds_read_b64_tr_b16 v[68:69], v115 offset:0x3800
	ds_read_b64_tr_b16 v[148:149], v115 offset:0x200
	ds_read_b64_tr_b16 v[150:151], v115 offset:0xa00
	ds_read_b64_tr_b16 v[152:153], v115 offset:0x1200
	ds_read_b64_tr_b16 v[154:155], v115 offset:0x1a00
	ds_read_b64_tr_b16 v[156:157], v115 offset:0x2200
	ds_read_b64_tr_b16 v[158:159], v115 offset:0x2a00
	ds_read_b64_tr_b16 v[160:161], v115 offset:0x3200
	ds_read_b64_tr_b16 v[162:163], v115 offset:0x3a00
	s_nop 0
	s_waitcnt lgkmcnt(8)
	s_nop 0
	v_mfma_f32_32x32x16_bf16 v[2:17], v[58:61], v[42:45], v[2:17]
	v_mfma_f32_32x32x16_bf16 v[2:17], v[38:41], v[46:49], v[2:17]
	v_mfma_f32_32x32x16_bf16 v[2:17], v[54:57], v[62:65], v[2:17]
	v_mfma_f32_32x32x16_bf16 v[2:17], v[50:53], v[66:69], v[2:17]
	s_waitcnt lgkmcnt(0)
	s_nop 0
	v_mfma_f32_32x32x16_bf16 v[18:33], v[58:61], v[148:151], v[18:33]
	s_barrier
	s_waitcnt vmcnt(7)
	v_and_b32_e32 v58, 0xffff0000, v108
	v_mul_f32_e32 v63, 0xbfb8aa3b, v58
	v_exp_f32_e32 v63, v63
	v_lshlrev_b32_e32 v59, 16, v109
	v_mfma_f32_32x32x16_bf16 v[18:33], v[38:41], v[152:155], v[18:33]
	v_add_u32_e32 v38, s27, v121
	v_add_u32_e32 v39, 0xa000, v38
	v_add_u32_e32 v40, 0xa400, v38
	v_add_u32_e32 v41, 0xa800, v38
	v_add_u32_e32 v42, 0xac00, v38
	v_add_u32_e32 v43, 0xc000, v38
	v_add_u32_e32 v44, 0xc400, v38
	v_mfma_f32_32x32x16_bf16 v[18:33], v[54:57], v[156:159], v[18:33]
	v_add_u32_e32 v45, 0xc800, v38
	v_add_u32_e32 v46, 0xcc00, v38
	v_add_u32_e32 v47, 0xe000, v38
	v_add_u32_e32 v48, 0xe400, v38
	v_add_u32_e32 v49, 0xe800, v38
	v_add_u32_e32 v54, 0x6000, v143
	v_add_u32_e32 v38, 0xec00, v38
	v_mfma_f32_32x32x16_bf16 v[18:33], v[50:53], v[160:163], v[18:33]
	v_and_b32_e32 v60, 0xffff0000, v109
	v_readlane_b32 s0, v254, 53
	s_nop 9
	ds_write2_b32 v39, v2, v18 offset1:32
	ds_write2_b32 v40, v3, v19 offset0:4 offset1:36
	ds_write2_b32 v41, v4, v20 offset0:8 offset1:40
	ds_write2_b32 v42, v5, v21 offset0:12 offset1:44
	ds_write2_b32 v43, v6, v22 offset0:32 offset1:64
	ds_write2_b32 v44, v7, v23 offset0:36 offset1:68
	ds_write2_b32 v45, v8, v24 offset0:40 offset1:72
	ds_write2_b32 v46, v9, v25 offset0:44 offset1:76
	ds_write2_b32 v47, v10, v26 offset0:64 offset1:96
	ds_write2_b32 v48, v11, v27 offset0:68 offset1:100
	ds_write2_b32 v49, v12, v28 offset0:72 offset1:104
	ds_write2_b32 v38, v13, v29 offset0:76 offset1:108
	ds_write2_b32 v54, v14, v30 offset0:96 offset1:128
	v_add_u32_e32 v2, 0x6400, v143
	ds_write2_b32 v2, v15, v31 offset0:100 offset1:132
	v_add_u32_e32 v2, 0x6800, v143
	ds_write2_b32 v2, v16, v32 offset0:104 offset1:136
	v_add_u32_e32 v2, 0x6c00, v143
	ds_write2_b32 v2, v17, v33 offset0:108 offset1:140
	s_waitcnt lgkmcnt(0)
	s_barrier
	ds_read_b128 v[30:33], v144 offset:40960
	ds_read_b128 v[26:29], v144 offset:42000
	ds_read_b128 v[22:25], v144 offset:43040
	ds_read_b128 v[18:21], v144 offset:44080
	ds_read_b128 v[14:17], v144 offset:45120
	ds_read_b128 v[10:13], v144 offset:46160
	s_waitcnt lgkmcnt(5)
	v_pk_mul_f32 v[4:5], v[30:31], v[30:31]
	v_pk_mul_f32 v[2:3], v[32:33], v[32:33]
	v_add_f32_e32 v4, v4, v5
	v_add_f32_e32 v2, v2, v4
	s_waitcnt lgkmcnt(4)
	v_pk_mul_f32 v[4:5], v[26:27], v[26:27]
	v_add_f32_e32 v42, v3, v2
	v_pk_mul_f32 v[2:3], v[28:29], v[28:29]
	v_add_f32_e32 v4, v4, v5
	v_add_f32_e32 v2, v2, v4
	s_waitcnt lgkmcnt(3)
	v_pk_mul_f32 v[4:5], v[22:23], v[22:23]
	v_add_f32_e32 v43, v3, v2
	v_pk_mul_f32 v[2:3], v[24:25], v[24:25]
	v_add_f32_e32 v4, v4, v5
	v_add_f32_e32 v2, v2, v4
	s_waitcnt lgkmcnt(2)
	v_pk_mul_f32 v[4:5], v[18:19], v[18:19]
	v_add_f32_e32 v44, v3, v2
	v_pk_mul_f32 v[2:3], v[20:21], v[20:21]
	v_add_f32_e32 v4, v4, v5
	v_add_f32_e32 v2, v2, v4
	s_waitcnt lgkmcnt(1)
	v_pk_mul_f32 v[4:5], v[14:15], v[14:15]
	v_add_f32_e32 v45, v3, v2
	v_pk_mul_f32 v[2:3], v[16:17], v[16:17]
	v_add_f32_e32 v4, v4, v5
	v_add_f32_e32 v2, v2, v4
	s_waitcnt lgkmcnt(0)
	v_pk_mul_f32 v[4:5], v[10:11], v[10:11]
	v_add_f32_e32 v46, v3, v2
	v_pk_mul_f32 v[2:3], v[12:13], v[12:13]
	ds_read_b128 v[6:9], v144 offset:47200
	v_add_f32_e32 v4, v4, v5
	v_add_f32_e32 v2, v2, v4
	v_add_f32_e32 v47, v3, v2
	ds_read_b128 v[2:5], v144 offset:48240
	s_waitcnt lgkmcnt(1)
	v_pk_mul_f32 v[40:41], v[6:7], v[6:7]
	v_pk_mul_f32 v[38:39], v[8:9], v[8:9]
	v_add_f32_e32 v40, v40, v41
	v_add_f32_e32 v38, v38, v40
	s_waitcnt lgkmcnt(0)
	v_pk_mul_f32 v[40:41], v[2:3], v[2:3]
	v_add_f32_e32 v54, v39, v38
	v_pk_mul_f32 v[38:39], v[4:5], v[4:5]
	v_add_f32_e32 v40, v40, v41
	v_add_f32_e32 v38, v38, v40
	v_add_f32_e32 v38, v39, v38
	v_add_f32_dpp v39, v42, v42 quad_perm:[1,0,3,2] row_mask:0xf bank_mask:0xf bound_ctrl:1
	v_add_f32_dpp v41, v43, v43 quad_perm:[1,0,3,2] row_mask:0xf bank_mask:0xf bound_ctrl:1
	v_add_f32_dpp v38, v38, v38 quad_perm:[1,0,3,2] row_mask:0xf bank_mask:0xf bound_ctrl:1
	v_add_f32_dpp v39, v39, v39 quad_perm:[2,3,0,1] row_mask:0xf bank_mask:0xf bound_ctrl:1
	v_add_f32_dpp v41, v41, v41 quad_perm:[2,3,0,1] row_mask:0xf bank_mask:0xf bound_ctrl:1
	v_add_f32_dpp v38, v38, v38 quad_perm:[2,3,0,1] row_mask:0xf bank_mask:0xf bound_ctrl:1
	v_add_f32_dpp v39, v39, v39 row_half_mirror row_mask:0xf bank_mask:0xf bound_ctrl:1
	v_add_f32_dpp v41, v41, v41 row_half_mirror row_mask:0xf bank_mask:0xf bound_ctrl:1
	v_add_f32_dpp v38, v38, v38 row_half_mirror row_mask:0xf bank_mask:0xf bound_ctrl:1
	v_add_f32_dpp v39, v39, v39 row_ror:8 row_mask:0xf bank_mask:0xf bound_ctrl:1
	ds_swizzle_b32 v40, v39 offset:swizzle(SWAP,16)
	v_add_f32_dpp v41, v41, v41 row_ror:8 row_mask:0xf bank_mask:0xf bound_ctrl:1
	ds_swizzle_b32 v42, v41 offset:swizzle(SWAP,16)
	v_add_f32_dpp v38, v38, v38 row_ror:8 row_mask:0xf bank_mask:0xf bound_ctrl:1
	s_waitcnt lgkmcnt(1)
	v_add_f32_e32 v43, v39, v40
	v_add_f32_dpp v39, v44, v44 quad_perm:[1,0,3,2] row_mask:0xf bank_mask:0xf bound_ctrl:1
	s_waitcnt lgkmcnt(0)
	v_add_f32_e32 v42, v41, v42
	v_add_f32_dpp v41, v45, v45 quad_perm:[1,0,3,2] row_mask:0xf bank_mask:0xf bound_ctrl:1
	v_add_f32_dpp v39, v39, v39 quad_perm:[2,3,0,1] row_mask:0xf bank_mask:0xf bound_ctrl:1
	v_mov_b32_e32 v53, v43
	v_mov_b32_e32 v52, v42
	v_add_f32_dpp v39, v39, v39 row_half_mirror row_mask:0xf bank_mask:0xf bound_ctrl:1
	v_permlane32_swap_b32_e32 v43, v53
	s_nop 0
	v_add_f32_dpp v39, v39, v39 row_ror:8 row_mask:0xf bank_mask:0xf bound_ctrl:1
	ds_swizzle_b32 v40, v39 offset:swizzle(SWAP,16)
	v_permlane32_swap_b32_e32 v42, v52
	v_pk_add_f32 v[52:53], v[42:43], v[52:53]
	v_add_f32_dpp v41, v41, v41 quad_perm:[2,3,0,1] row_mask:0xf bank_mask:0xf bound_ctrl:1
	s_waitcnt lgkmcnt(0)
	v_add_f32_e32 v49, v39, v40
	v_add_f32_dpp v39, v46, v46 quad_perm:[1,0,3,2] row_mask:0xf bank_mask:0xf bound_ctrl:1
	v_add_f32_dpp v41, v41, v41 row_half_mirror row_mask:0xf bank_mask:0xf bound_ctrl:1
	v_mov_b32_e32 v51, v49
	v_add_f32_dpp v39, v39, v39 quad_perm:[2,3,0,1] row_mask:0xf bank_mask:0xf bound_ctrl:1
	v_add_f32_dpp v41, v41, v41 row_ror:8 row_mask:0xf bank_mask:0xf bound_ctrl:1
	ds_swizzle_b32 v44, v41 offset:swizzle(SWAP,16)
	v_add_f32_dpp v39, v39, v39 row_half_mirror row_mask:0xf bank_mask:0xf bound_ctrl:1
	v_permlane32_swap_b32_e32 v49, v51
	s_nop 0
	v_add_f32_dpp v39, v39, v39 row_ror:8 row_mask:0xf bank_mask:0xf bound_ctrl:1
	ds_swizzle_b32 v40, v39 offset:swizzle(SWAP,16)
	s_waitcnt lgkmcnt(1)
	v_add_f32_e32 v48, v41, v44
	v_mov_b32_e32 v50, v48
	s_nop 1
	v_permlane32_swap_b32_e32 v48, v50
	s_waitcnt lgkmcnt(0)
	v_add_f32_e32 v45, v39, v40
	v_add_f32_dpp v39, v54, v54 quad_perm:[1,0,3,2] row_mask:0xf bank_mask:0xf bound_ctrl:1
	ds_swizzle_b32 v54, v38 offset:swizzle(SWAP,16)
	v_add_f32_dpp v41, v47, v47 quad_perm:[1,0,3,2] row_mask:0xf bank_mask:0xf bound_ctrl:1
	v_add_f32_dpp v39, v39, v39 quad_perm:[2,3,0,1] row_mask:0xf bank_mask:0xf bound_ctrl:1
	v_mov_b32_e32 v47, v45
	v_add_f32_dpp v41, v41, v41 quad_perm:[2,3,0,1] row_mask:0xf bank_mask:0xf bound_ctrl:1
	v_add_f32_dpp v39, v39, v39 row_half_mirror row_mask:0xf bank_mask:0xf bound_ctrl:1
	s_waitcnt lgkmcnt(0)
	v_add_f32_e32 v38, v38, v54
	v_lshlrev_b32_e32 v54, 16, v108
	v_add_f32_dpp v39, v39, v39 row_ror:8 row_mask:0xf bank_mask:0xf bound_ctrl:1
	ds_swizzle_b32 v40, v39 offset:swizzle(SWAP,16)
	v_add_f32_dpp v41, v41, v41 row_half_mirror row_mask:0xf bank_mask:0xf bound_ctrl:1
	v_permlane32_swap_b32_e32 v45, v47
	s_nop 0
	v_add_f32_dpp v41, v41, v41 row_ror:8 row_mask:0xf bank_mask:0xf bound_ctrl:1
	s_waitcnt lgkmcnt(0)
	v_add_f32_e32 v39, v39, v40
	v_mul_f32_e32 v40, 0xbfb8aa3b, v54
	v_exp_f32_e32 v55, v40
	ds_swizzle_b32 v44, v41 offset:swizzle(SWAP,16)
	v_mov_b32_e32 v40, v38
	s_nop 1
	v_permlane32_swap_b32_e32 v38, v40
	v_add_f32_e32 v55, 1.0, v55
	v_div_scale_f32 v56, vcc, v55, v55, v54
	v_rcp_f32_e32 v57, v56
	s_waitcnt lgkmcnt(0)
	v_add_f32_e32 v44, v41, v44
	v_mov_b32_e32 v46, v44
	s_nop 1
	v_permlane32_swap_b32_e32 v44, v46
	v_fma_f32 v61, -v56, v57, 1.0
	v_fmac_f32_e32 v57, v61, v57
	v_div_scale_f32 v61, vcc, v54, v55, v54
	v_mul_f32_e32 v62, v61, v57
	v_fma_f32 v64, -v56, v62, v61
	v_fmac_f32_e32 v62, v64, v57
	v_fma_f32 v56, -v56, v62, v61
	v_add_f32_e32 v61, 1.0, v63
	v_div_scale_f32 v63, s[30:31], v61, v61, v58
	v_rcp_f32_e32 v64, v63
	v_div_fmas_f32 v56, v56, v57, v62
	v_mul_f32_e32 v57, 0xbfb8aa3b, v59
	v_exp_f32_e32 v57, v57
	v_div_fixup_f32 v56, v56, v55, v54
	v_fma_f32 v54, -v63, v64, 1.0
	v_fmac_f32_e32 v64, v54, v64
	v_div_scale_f32 v54, vcc, v58, v61, v58
	v_mul_f32_e32 v55, v54, v64
	v_fma_f32 v62, -v63, v55, v54
	v_add_f32_e32 v57, 1.0, v57
	v_fmac_f32_e32 v55, v62, v64
	v_div_scale_f32 v62, s[30:31], v57, v57, v59
	v_fma_f32 v54, -v63, v55, v54
	v_rcp_f32_e32 v63, v62
	v_div_fmas_f32 v54, v54, v64, v55
	v_div_fixup_f32 v58, v54, v61, v58
	v_mul_f32_e32 v61, 0xbfb8aa3b, v60
	v_fma_f32 v54, -v62, v63, 1.0
	v_exp_f32_e32 v61, v61
	v_fmac_f32_e32 v63, v54, v63
	v_div_scale_f32 v54, vcc, v59, v57, v59
	v_mul_f32_e32 v55, v54, v63
	v_fma_f32 v64, -v62, v55, v54
	v_fmac_f32_e32 v55, v64, v63
	v_add_f32_e32 v61, 1.0, v61
	v_fma_f32 v54, -v62, v55, v54
	v_div_scale_f32 v62, s[30:31], v61, v61, v60
	v_rcp_f32_e32 v64, v62
	v_div_fmas_f32 v54, v54, v63, v55
	v_div_fixup_f32 v57, v54, v57, v59
	s_lshl_b64 s[30:31], s[74:75], 12
	v_fma_f32 v54, -v62, v64, 1.0
	v_fmac_f32_e32 v64, v54, v64
	v_div_scale_f32 v54, vcc, v60, v61, v60
	v_mul_f32_e32 v55, v54, v64
	v_fma_f32 v59, -v62, v55, v54
	v_fmac_f32_e32 v55, v59, v64
	s_add_u32 s25, s96, s30
	s_mov_b32 s30, 0x358637bd
	v_fma_f32 v54, -v62, v55, v54
	v_mov_b64_e32 v[42:43], s[30:31]
	v_div_fmas_f32 v54, v54, v64, v55
	v_pk_fma_f32 v[52:53], v[52:53], s[26:27], v[42:43] op_sel_hi:[1,0,0]
	v_div_fixup_f32 v59, v54, v61, v60
	v_mul_f32_e32 v54, 0x4b800000, v53
	v_cmp_gt_f32_e32 vcc, s21, v53
	s_addc_u32 s29, s97, s31
	s_add_u32 s30, s25, s4
	v_cndmask_b32_e32 v53, v53, v54, vcc
	v_rsq_f32_e32 v53, v53
	s_addc_u32 s31, s29, 0
	v_lshl_add_u64 v[54:55], s[30:31], 0, v[92:93]
	v_mov_b32_e32 v41, v39
	v_mul_f32_e32 v60, 0x45800000, v53
	v_cndmask_b32_e32 v53, v53, v60, vcc
	v_mul_f32_e32 v30, v30, v53
	v_mul_f32_e32 v31, v31, v53
	v_mul_f32_e32 v30, v34, v30
	v_mul_f32_e32 v31, v35, v31
	v_mul_f32_e32 v30, v56, v30
	v_mul_f32_e32 v31, v58, v31
	v_cvt_pk_bf16_f32 v30, v30, v31
	v_mul_f32_e32 v31, v32, v53
	v_mul_f32_e32 v32, v33, v53
	v_mul_f32_e32 v31, v36, v31
	v_mul_f32_e32 v32, v37, v32
	v_mul_f32_e32 v31, v57, v31
	v_mul_f32_e32 v32, v59, v32
	v_cvt_pk_bf16_f32 v31, v31, v32
	v_mul_f32_e32 v32, 0x4b800000, v52
	v_cmp_gt_f32_e32 vcc, s21, v52
	v_permlane32_swap_b32_e32 v39, v41
	s_nop 0
	v_cndmask_b32_e32 v32, v52, v32, vcc
	v_rsq_f32_e32 v52, v32
	v_add_co_u32_e64 v32, s[74:75], s24, v54
	s_nop 1
	v_addc_co_u32_e64 v33, s[74:75], 0, v55, s[74:75]
	global_store_dwordx2 v[32:33], v[30:31], off offset:2048
	s_waitcnt vmcnt(7)
	v_lshlrev_b32_e32 v31, 16, v106
	v_mul_f32_e32 v32, 0xbfb8aa3b, v31
	v_exp_f32_e32 v32, v32
	v_mul_f32_e32 v30, 0x45800000, v52
	v_cndmask_b32_e32 v30, v52, v30, vcc
	v_and_b32_e32 v33, 0xffff0000, v106
	v_add_f32_e32 v32, 1.0, v32
	v_div_scale_f32 v53, s[30:31], v32, v32, v31
	v_rcp_f32_e32 v54, v53
	v_mul_f32_e32 v26, v26, v30
	v_mul_f32_e32 v26, v34, v26
	v_lshlrev_b32_e32 v52, 16, v107
	v_fma_f32 v56, -v53, v54, 1.0
	v_fmac_f32_e32 v54, v56, v54
	v_div_scale_f32 v56, vcc, v31, v32, v31
	v_mul_f32_e32 v57, v56, v54
	v_fma_f32 v58, -v53, v57, v56
	v_fmac_f32_e32 v57, v58, v54
	v_fma_f32 v53, -v53, v57, v56
	v_mul_f32_e32 v56, 0xbfb8aa3b, v33
	v_exp_f32_e32 v56, v56
	v_div_fmas_f32 v53, v53, v54, v57
	v_div_fixup_f32 v31, v53, v32, v31
	v_mul_f32_e32 v26, v31, v26
	v_add_f32_e32 v32, 1.0, v56
	v_div_scale_f32 v53, s[30:31], v32, v32, v33
	v_rcp_f32_e32 v54, v53
	v_mul_f32_e32 v27, v27, v30
	v_mul_f32_e32 v27, v35, v27
	v_and_b32_e32 v55, 0xffff0000, v107
	v_fma_f32 v31, -v53, v54, 1.0
	v_fmac_f32_e32 v54, v31, v54
	v_div_scale_f32 v31, vcc, v33, v32, v33
	v_mul_f32_e32 v56, v31, v54
	v_fma_f32 v57, -v53, v56, v31
	v_fmac_f32_e32 v56, v57, v54
	v_fma_f32 v31, -v53, v56, v31
	v_mul_f32_e32 v53, 0xbfb8aa3b, v52
	v_exp_f32_e32 v53, v53
	v_div_fmas_f32 v31, v31, v54, v56
	v_div_fixup_f32 v31, v31, v32, v33
	v_mul_f32_e32 v27, v31, v27
	v_add_f32_e32 v31, 1.0, v53
	v_div_scale_f32 v32, s[30:31], v31, v31, v52
	v_rcp_f32_e32 v33, v32
	v_cvt_pk_bf16_f32 v26, v26, v27
	v_mul_f32_e32 v27, v28, v30
	v_mul_f32_e32 v27, v36, v27
	v_fma_f32 v28, -v32, v33, 1.0
	v_fmac_f32_e32 v33, v28, v33
	v_div_scale_f32 v28, vcc, v52, v31, v52
	v_mul_f32_e32 v53, v28, v33
	v_fma_f32 v54, -v32, v53, v28
	v_fmac_f32_e32 v53, v54, v33
	v_fma_f32 v28, -v32, v53, v28
	v_mul_f32_e32 v32, 0xbfb8aa3b, v55
	v_exp_f32_e32 v32, v32
	v_div_fmas_f32 v28, v28, v33, v53
	v_div_fixup_f32 v28, v28, v31, v52
	v_mul_f32_e32 v27, v28, v27
	v_add_f32_e32 v31, 1.0, v32
	v_div_scale_f32 v32, s[30:31], v31, v31, v55
	v_rcp_f32_e32 v33, v32
	v_mul_f32_e32 v28, v29, v30
	s_lshl_b64 s[30:31], s[94:95], 12
	s_add_u32 s25, s96, s30
	v_fma_f32 v29, -v32, v33, 1.0
	v_fmac_f32_e32 v33, v29, v33
	v_div_scale_f32 v29, vcc, v55, v31, v55
	v_mul_f32_e32 v30, v29, v33
	v_fma_f32 v52, -v32, v30, v29
	v_fmac_f32_e32 v30, v52, v33
	v_fma_f32 v29, -v32, v30, v29
	v_div_fmas_f32 v29, v29, v33, v30
	s_addc_u32 s29, s97, s31
	s_waitcnt vmcnt(6)
	v_lshlrev_b32_e32 v30, 16, v104
	v_mul_f32_e32 v28, v37, v28
	v_div_fixup_f32 v29, v29, v31, v55
	s_add_u32 s30, s25, s4
	v_mul_f32_e32 v31, 0xbfb8aa3b, v30
	v_mul_f32_e32 v28, v29, v28
	s_addc_u32 s31, s29, 0
	v_exp_f32_e32 v31, v31
	v_cvt_pk_bf16_f32 v27, v27, v28
	v_lshl_add_u64 v[28:29], s[30:31], 0, v[92:93]
	v_add_co_u32_e32 v28, vcc, s24, v28
	v_and_b32_e32 v32, 0xffff0000, v105
	s_nop 0
	v_addc_co_u32_e32 v29, vcc, 0, v29, vcc
	global_store_dwordx2 v[28:29], v[26:27], off offset:2048
	v_add_f32_e32 v26, 1.0, v31
	v_div_scale_f32 v27, s[30:31], v26, v26, v30
	v_rcp_f32_e32 v28, v27
	v_and_b32_e32 v29, 0xffff0000, v104
	v_mul_f32_e32 v53, 0xbfb8aa3b, v29
	v_exp_f32_e32 v53, v53
	v_fma_f32 v33, -v27, v28, 1.0
	v_fmac_f32_e32 v28, v33, v28
	v_div_scale_f32 v33, vcc, v30, v26, v30
	v_mul_f32_e32 v52, v33, v28
	v_fma_f32 v54, -v27, v52, v33
	v_fmac_f32_e32 v52, v54, v28
	v_fma_f32 v27, -v27, v52, v33
	v_add_f32_e32 v33, 1.0, v53
	v_div_scale_f32 v53, s[30:31], v33, v33, v29
	v_rcp_f32_e32 v54, v53
	v_lshlrev_b32_e32 v31, 16, v105
	v_div_fmas_f32 v27, v27, v28, v52
	v_mul_f32_e32 v28, 0xbfb8aa3b, v31
	v_exp_f32_e32 v28, v28
	v_div_fixup_f32 v30, v27, v26, v30
	v_fma_f32 v26, -v53, v54, 1.0
	v_fmac_f32_e32 v54, v26, v54
	v_div_scale_f32 v26, vcc, v29, v33, v29
	v_mul_f32_e32 v27, v26, v54
	v_fma_f32 v52, -v53, v27, v26
	v_add_f32_e32 v28, 1.0, v28
	v_fmac_f32_e32 v27, v52, v54
	v_div_scale_f32 v52, s[30:31], v28, v28, v31
	v_fma_f32 v26, -v53, v27, v26
	v_rcp_f32_e32 v53, v52
	v_div_fmas_f32 v26, v26, v54, v27
	v_div_fixup_f32 v33, v26, v33, v29
	v_mul_f32_e32 v29, 0xbfb8aa3b, v32
	v_fma_f32 v26, -v52, v53, 1.0
	v_exp_f32_e32 v29, v29
	v_fmac_f32_e32 v53, v26, v53
	v_div_scale_f32 v26, vcc, v31, v28, v31
	v_mul_f32_e32 v27, v26, v53
	v_fma_f32 v54, -v52, v27, v26
	v_fmac_f32_e32 v27, v54, v53
	v_add_f32_e32 v29, 1.0, v29
	v_fma_f32 v26, -v52, v27, v26
	v_div_scale_f32 v52, s[30:31], v29, v29, v32
	v_rcp_f32_e32 v54, v52
	v_div_fmas_f32 v26, v26, v53, v27
	v_div_fixup_f32 v31, v26, v28, v31
	s_lshl_b64 s[12:13], s[12:13], 12
	v_fma_f32 v26, -v52, v54, 1.0
	v_fmac_f32_e32 v54, v26, v54
	v_div_scale_f32 v26, vcc, v32, v29, v32
	v_mul_f32_e32 v27, v26, v54
	v_fma_f32 v28, -v52, v27, v26
	v_fmac_f32_e32 v27, v28, v54
	v_fma_f32 v26, -v52, v27, v26
	v_div_fmas_f32 v26, v26, v54, v27
	v_div_fixup_f32 v32, v26, v29, v32
	v_pk_add_f32 v[26:27], v[48:49], v[50:51]
	s_add_u32 s12, s96, s12
	v_pk_fma_f32 v[26:27], v[26:27], s[26:27], v[42:43] op_sel_hi:[1,0,0]
	s_addc_u32 s13, s97, s13
	v_mul_f32_e32 v28, 0x4b800000, v27
	v_cmp_gt_f32_e32 vcc, s21, v27
	s_add_u32 s12, s12, s4
	s_addc_u32 s13, s13, 0
	v_cndmask_b32_e32 v27, v27, v28, vcc
	v_rsq_f32_e32 v27, v27
	v_lshl_add_u64 v[28:29], s[12:13], 0, v[92:93]
	s_lshl_b64 s[10:11], s[10:11], 12
	s_add_u32 s10, s96, s10
	v_mul_f32_e32 v48, 0x45800000, v27
	v_cndmask_b32_e32 v27, v27, v48, vcc
	v_mul_f32_e32 v22, v22, v27
	v_mul_f32_e32 v23, v23, v27
	v_mul_f32_e32 v22, v34, v22
	v_mul_f32_e32 v23, v35, v23
	v_mul_f32_e32 v22, v30, v22
	v_mul_f32_e32 v23, v33, v23
	v_cvt_pk_bf16_f32 v22, v22, v23
	v_mul_f32_e32 v23, v24, v27
	v_mul_f32_e32 v24, v25, v27
	v_mul_f32_e32 v23, v36, v23
	v_mul_f32_e32 v24, v37, v24
	v_mul_f32_e32 v23, v31, v23
	v_mul_f32_e32 v24, v32, v24
	v_cvt_pk_bf16_f32 v23, v23, v24
	v_mul_f32_e32 v24, 0x4b800000, v26
	v_cmp_gt_f32_e32 vcc, s21, v26
	s_addc_u32 s11, s97, s11
	s_add_u32 s10, s10, s4
	v_cndmask_b32_e32 v24, v26, v24, vcc
	v_rsq_f32_e32 v26, v24
	v_add_co_u32_e64 v24, s[74:75], s24, v28
	s_addc_u32 s11, s11, 0
	s_nop 0
	v_addc_co_u32_e64 v25, s[74:75], 0, v29, s[74:75]
	global_store_dwordx2 v[24:25], v[22:23], off offset:2048
	s_waitcnt vmcnt(7)
	v_lshlrev_b32_e32 v23, 16, v100
	v_mul_f32_e32 v24, 0xbfb8aa3b, v23
	v_exp_f32_e32 v24, v24
	v_mul_f32_e32 v22, 0x45800000, v26
	v_cndmask_b32_e32 v22, v26, v22, vcc
	v_and_b32_e32 v25, 0xffff0000, v100
	v_add_f32_e32 v24, 1.0, v24
	v_div_scale_f32 v27, s[12:13], v24, v24, v23
	v_rcp_f32_e32 v28, v27
	v_mul_f32_e32 v18, v18, v22
	v_mul_f32_e32 v18, v34, v18
	v_lshlrev_b32_e32 v26, 16, v101
	v_fma_f32 v30, -v27, v28, 1.0
	v_fmac_f32_e32 v28, v30, v28
	v_div_scale_f32 v30, vcc, v23, v24, v23
	v_mul_f32_e32 v31, v30, v28
	v_fma_f32 v32, -v27, v31, v30
	v_fmac_f32_e32 v31, v32, v28
	v_fma_f32 v27, -v27, v31, v30
	v_mul_f32_e32 v30, 0xbfb8aa3b, v25
	v_exp_f32_e32 v30, v30
	v_div_fmas_f32 v27, v27, v28, v31
	v_div_fixup_f32 v23, v27, v24, v23
	v_mul_f32_e32 v18, v23, v18
	v_add_f32_e32 v24, 1.0, v30
	v_div_scale_f32 v27, s[12:13], v24, v24, v25
	v_rcp_f32_e32 v28, v27
	v_mul_f32_e32 v19, v19, v22
	v_mul_f32_e32 v19, v35, v19
	v_and_b32_e32 v29, 0xffff0000, v101
	v_fma_f32 v23, -v27, v28, 1.0
	v_fmac_f32_e32 v28, v23, v28
	v_div_scale_f32 v23, vcc, v25, v24, v25
	v_mul_f32_e32 v30, v23, v28
	v_fma_f32 v31, -v27, v30, v23
	v_fmac_f32_e32 v30, v31, v28
	v_fma_f32 v23, -v27, v30, v23
	v_mul_f32_e32 v27, 0xbfb8aa3b, v26
	v_exp_f32_e32 v27, v27
	v_div_fmas_f32 v23, v23, v28, v30
	v_div_fixup_f32 v23, v23, v24, v25
	v_mul_f32_e32 v19, v23, v19
	v_add_f32_e32 v23, 1.0, v27
	v_div_scale_f32 v24, s[12:13], v23, v23, v26
	v_rcp_f32_e32 v25, v24
	v_cvt_pk_bf16_f32 v18, v18, v19
	v_mul_f32_e32 v19, v20, v22
	v_mul_f32_e32 v19, v36, v19
	v_fma_f32 v20, -v24, v25, 1.0
	v_fmac_f32_e32 v25, v20, v25
	v_div_scale_f32 v20, vcc, v26, v23, v26
	v_mul_f32_e32 v27, v20, v25
	v_fma_f32 v28, -v24, v27, v20
	v_fmac_f32_e32 v27, v28, v25
	v_fma_f32 v20, -v24, v27, v20
	v_mul_f32_e32 v24, 0xbfb8aa3b, v29
	v_exp_f32_e32 v24, v24
	v_div_fmas_f32 v20, v20, v25, v27
	v_div_fixup_f32 v20, v20, v23, v26
	v_mul_f32_e32 v19, v20, v19
	v_add_f32_e32 v23, 1.0, v24
	v_div_scale_f32 v24, s[12:13], v23, v23, v29
	v_rcp_f32_e32 v25, v24
	v_mul_f32_e32 v20, v21, v22
	v_mul_f32_e32 v20, v37, v20
	s_lshl_b64 s[8:9], s[8:9], 12
	v_fma_f32 v21, -v24, v25, 1.0
	v_fmac_f32_e32 v25, v21, v25
	v_div_scale_f32 v21, vcc, v29, v23, v29
	v_mul_f32_e32 v22, v21, v25
	v_fma_f32 v26, -v24, v22, v21
	v_fmac_f32_e32 v22, v26, v25
	v_fma_f32 v21, -v24, v22, v21
	v_div_fmas_f32 v21, v21, v25, v22
	s_waitcnt vmcnt(6)
	v_lshlrev_b32_e32 v22, 16, v102
	v_div_fixup_f32 v21, v21, v23, v29
	v_mul_f32_e32 v23, 0xbfb8aa3b, v22
	v_mul_f32_e32 v20, v21, v20
	v_exp_f32_e32 v23, v23
	v_cvt_pk_bf16_f32 v19, v19, v20
	v_lshl_add_u64 v[20:21], s[10:11], 0, v[92:93]
	v_add_co_u32_e32 v20, vcc, s24, v20
	v_and_b32_e32 v24, 0xffff0000, v103
	s_nop 0
	v_addc_co_u32_e32 v21, vcc, 0, v21, vcc
	global_store_dwordx2 v[20:21], v[18:19], off offset:2048
	v_add_f32_e32 v18, 1.0, v23
	v_div_scale_f32 v19, s[10:11], v18, v18, v22
	v_rcp_f32_e32 v20, v19
	v_and_b32_e32 v21, 0xffff0000, v102
	v_mul_f32_e32 v27, 0xbfb8aa3b, v21
	v_exp_f32_e32 v27, v27
	v_fma_f32 v25, -v19, v20, 1.0
	v_fmac_f32_e32 v20, v25, v20
	v_div_scale_f32 v25, vcc, v22, v18, v22
	v_mul_f32_e32 v26, v25, v20
	v_fma_f32 v28, -v19, v26, v25
	v_fmac_f32_e32 v26, v28, v20
	v_fma_f32 v19, -v19, v26, v25
	v_add_f32_e32 v25, 1.0, v27
	v_div_scale_f32 v27, s[10:11], v25, v25, v21
	v_rcp_f32_e32 v28, v27
	v_lshlrev_b32_e32 v23, 16, v103
	v_div_fmas_f32 v19, v19, v20, v26
	v_mul_f32_e32 v20, 0xbfb8aa3b, v23
	v_exp_f32_e32 v20, v20
	v_div_fixup_f32 v22, v19, v18, v22
	v_fma_f32 v18, -v27, v28, 1.0
	v_fmac_f32_e32 v28, v18, v28
	v_div_scale_f32 v18, vcc, v21, v25, v21
	v_mul_f32_e32 v19, v18, v28
	v_fma_f32 v26, -v27, v19, v18
	v_add_f32_e32 v20, 1.0, v20
	v_fmac_f32_e32 v19, v26, v28
	v_div_scale_f32 v26, s[10:11], v20, v20, v23
	v_fma_f32 v18, -v27, v19, v18
	v_rcp_f32_e32 v27, v26
	v_div_fmas_f32 v18, v18, v28, v19
	v_div_fixup_f32 v25, v18, v25, v21
	v_mul_f32_e32 v21, 0xbfb8aa3b, v24
	v_fma_f32 v18, -v26, v27, 1.0
	v_exp_f32_e32 v21, v21
	v_fmac_f32_e32 v27, v18, v27
	v_div_scale_f32 v18, vcc, v23, v20, v23
	v_mul_f32_e32 v19, v18, v27
	v_fma_f32 v28, -v26, v19, v18
	v_fmac_f32_e32 v19, v28, v27
	v_add_f32_e32 v21, 1.0, v21
	v_fma_f32 v18, -v26, v19, v18
	v_div_scale_f32 v26, s[10:11], v21, v21, v24
	v_rcp_f32_e32 v28, v26
	v_div_fmas_f32 v18, v18, v27, v19
	v_div_fixup_f32 v23, v18, v20, v23
	s_add_u32 s8, s96, s8
	v_fma_f32 v18, -v26, v28, 1.0
	v_fmac_f32_e32 v28, v18, v28
	v_div_scale_f32 v18, vcc, v24, v21, v24
	v_mul_f32_e32 v19, v18, v28
	v_fma_f32 v20, -v26, v19, v18
	v_fmac_f32_e32 v19, v20, v28
	v_fma_f32 v18, -v26, v19, v18
	v_div_fmas_f32 v18, v18, v28, v19
	v_div_fixup_f32 v24, v18, v21, v24
	v_pk_add_f32 v[18:19], v[44:45], v[46:47]
	s_addc_u32 s9, s97, s9
	v_pk_fma_f32 v[18:19], v[18:19], s[26:27], v[42:43] op_sel_hi:[1,0,0]
	s_add_u32 s8, s8, s4
	v_mul_f32_e32 v20, 0x4b800000, v19
	v_cmp_gt_f32_e32 vcc, s21, v19
	s_addc_u32 s9, s9, 0
	s_nop 0
	v_cndmask_b32_e32 v19, v19, v20, vcc
	v_rsq_f32_e32 v19, v19
	v_lshl_add_u64 v[20:21], s[8:9], 0, v[92:93]
	v_mul_f32_e32 v26, 0x45800000, v19
	v_cndmask_b32_e32 v19, v19, v26, vcc
	v_mul_f32_e32 v14, v14, v19
	v_mul_f32_e32 v15, v15, v19
	v_mul_f32_e32 v14, v34, v14
	v_mul_f32_e32 v15, v35, v15
	v_mul_f32_e32 v14, v22, v14
	v_mul_f32_e32 v15, v25, v15
	v_cvt_pk_bf16_f32 v14, v14, v15
	v_mul_f32_e32 v15, v16, v19
	v_mul_f32_e32 v16, v17, v19
	v_mul_f32_e32 v15, v36, v15
	v_mul_f32_e32 v16, v37, v16
	v_mul_f32_e32 v15, v23, v15
	v_mul_f32_e32 v16, v24, v16
	v_cvt_pk_bf16_f32 v15, v15, v16
	v_mul_f32_e32 v16, 0x4b800000, v18
	v_cmp_gt_f32_e32 vcc, s21, v18
	s_nop 1
	v_cndmask_b32_e32 v16, v18, v16, vcc
	v_rsq_f32_e32 v18, v16
	v_add_co_u32_e64 v16, s[74:75], s24, v20
	s_nop 1
	v_addc_co_u32_e64 v17, s[74:75], 0, v21, s[74:75]
	global_store_dwordx2 v[16:17], v[14:15], off offset:2048
	s_waitcnt vmcnt(7)
	v_lshlrev_b32_e32 v15, 16, v98
	v_mul_f32_e32 v16, 0xbfb8aa3b, v15
	v_exp_f32_e32 v16, v16
	v_mul_f32_e32 v14, 0x45800000, v18
	v_cndmask_b32_e32 v14, v18, v14, vcc
	v_and_b32_e32 v17, 0xffff0000, v98
	v_add_f32_e32 v16, 1.0, v16
	v_div_scale_f32 v19, s[8:9], v16, v16, v15
	v_rcp_f32_e32 v20, v19
	v_mul_f32_e32 v10, v10, v14
	v_mul_f32_e32 v10, v34, v10
	v_lshlrev_b32_e32 v18, 16, v99
	v_fma_f32 v22, -v19, v20, 1.0
	v_fmac_f32_e32 v20, v22, v20
	v_div_scale_f32 v22, vcc, v15, v16, v15
	v_mul_f32_e32 v23, v22, v20
	v_fma_f32 v24, -v19, v23, v22
	v_fmac_f32_e32 v23, v24, v20
	v_fma_f32 v19, -v19, v23, v22
	v_mul_f32_e32 v22, 0xbfb8aa3b, v17
	v_exp_f32_e32 v22, v22
	v_div_fmas_f32 v19, v19, v20, v23
	v_div_fixup_f32 v15, v19, v16, v15
	v_mul_f32_e32 v10, v15, v10
	v_add_f32_e32 v16, 1.0, v22
	v_div_scale_f32 v19, s[8:9], v16, v16, v17
	v_rcp_f32_e32 v20, v19
	v_mul_f32_e32 v11, v11, v14
	v_mul_f32_e32 v11, v35, v11
	v_and_b32_e32 v21, 0xffff0000, v99
	v_fma_f32 v15, -v19, v20, 1.0
	v_fmac_f32_e32 v20, v15, v20
	v_div_scale_f32 v15, vcc, v17, v16, v17
	v_mul_f32_e32 v22, v15, v20
	v_fma_f32 v23, -v19, v22, v15
	v_fmac_f32_e32 v22, v23, v20
	v_fma_f32 v15, -v19, v22, v15
	v_mul_f32_e32 v19, 0xbfb8aa3b, v18
	v_exp_f32_e32 v19, v19
	v_div_fmas_f32 v15, v15, v20, v22
	v_div_fixup_f32 v15, v15, v16, v17
	v_mul_f32_e32 v11, v15, v11
	v_add_f32_e32 v15, 1.0, v19
	v_div_scale_f32 v16, s[8:9], v15, v15, v18
	v_rcp_f32_e32 v17, v16
	v_cvt_pk_bf16_f32 v10, v10, v11
	v_mul_f32_e32 v11, v12, v14
	v_mul_f32_e32 v11, v36, v11
	v_fma_f32 v12, -v16, v17, 1.0
	v_fmac_f32_e32 v17, v12, v17
	v_div_scale_f32 v12, vcc, v18, v15, v18
	v_mul_f32_e32 v19, v12, v17
	v_fma_f32 v20, -v16, v19, v12
	v_fmac_f32_e32 v19, v20, v17
	v_fma_f32 v12, -v16, v19, v12
	v_mul_f32_e32 v16, 0xbfb8aa3b, v21
	v_exp_f32_e32 v16, v16
	v_div_fmas_f32 v12, v12, v17, v19
	v_div_fixup_f32 v12, v12, v15, v18
	v_mul_f32_e32 v11, v12, v11
	v_add_f32_e32 v15, 1.0, v16
	v_div_scale_f32 v16, s[8:9], v15, v15, v21
	v_rcp_f32_e32 v17, v16
	v_mul_f32_e32 v12, v13, v14
	s_lshl_b64 s[8:9], s[92:93], 12
	s_add_u32 s8, s96, s8
	v_fma_f32 v13, -v16, v17, 1.0
	v_fmac_f32_e32 v17, v13, v17
	v_div_scale_f32 v13, vcc, v21, v15, v21
	v_mul_f32_e32 v14, v13, v17
	v_fma_f32 v18, -v16, v14, v13
	v_fmac_f32_e32 v14, v18, v17
	v_fma_f32 v13, -v16, v14, v13
	v_div_fmas_f32 v13, v13, v17, v14
	s_addc_u32 s9, s97, s9
	s_waitcnt vmcnt(6)
	v_lshlrev_b32_e32 v14, 16, v96
	v_mul_f32_e32 v12, v37, v12
	v_div_fixup_f32 v13, v13, v15, v21
	s_add_u32 s8, s8, s4
	v_mul_f32_e32 v15, 0xbfb8aa3b, v14
	v_mul_f32_e32 v12, v13, v12
	s_addc_u32 s9, s9, 0
	v_exp_f32_e32 v15, v15
	v_cvt_pk_bf16_f32 v11, v11, v12
	v_lshl_add_u64 v[12:13], s[8:9], 0, v[92:93]
	v_add_co_u32_e32 v12, vcc, s24, v12
	v_and_b32_e32 v16, 0xffff0000, v97
	s_nop 0
	v_addc_co_u32_e32 v13, vcc, 0, v13, vcc
	global_store_dwordx2 v[12:13], v[10:11], off offset:2048
	v_add_f32_e32 v10, 1.0, v15
	v_div_scale_f32 v11, s[8:9], v10, v10, v14
	v_rcp_f32_e32 v12, v11
	v_and_b32_e32 v13, 0xffff0000, v96
	v_mul_f32_e32 v19, 0xbfb8aa3b, v13
	v_exp_f32_e32 v19, v19
	v_fma_f32 v17, -v11, v12, 1.0
	v_fmac_f32_e32 v12, v17, v12
	v_div_scale_f32 v17, vcc, v14, v10, v14
	v_mul_f32_e32 v18, v17, v12
	v_fma_f32 v20, -v11, v18, v17
	v_fmac_f32_e32 v18, v20, v12
	v_fma_f32 v11, -v11, v18, v17
	v_add_f32_e32 v17, 1.0, v19
	v_div_scale_f32 v19, s[8:9], v17, v17, v13
	v_rcp_f32_e32 v20, v19
	v_lshlrev_b32_e32 v15, 16, v97
	v_div_fmas_f32 v11, v11, v12, v18
	v_mul_f32_e32 v12, 0xbfb8aa3b, v15
	v_exp_f32_e32 v12, v12
	v_div_fixup_f32 v14, v11, v10, v14
	v_fma_f32 v10, -v19, v20, 1.0
	v_fmac_f32_e32 v20, v10, v20
	v_div_scale_f32 v10, vcc, v13, v17, v13
	v_mul_f32_e32 v11, v10, v20
	v_fma_f32 v18, -v19, v11, v10
	v_add_f32_e32 v12, 1.0, v12
	v_fmac_f32_e32 v11, v18, v20
	v_div_scale_f32 v18, s[8:9], v12, v12, v15
	v_fma_f32 v10, -v19, v11, v10
	v_rcp_f32_e32 v19, v18
	v_div_fmas_f32 v10, v10, v20, v11
	v_div_fixup_f32 v17, v10, v17, v13
	v_mul_f32_e32 v13, 0xbfb8aa3b, v16
	v_fma_f32 v10, -v18, v19, 1.0
	v_exp_f32_e32 v13, v13
	v_fmac_f32_e32 v19, v10, v19
	v_div_scale_f32 v10, vcc, v15, v12, v15
	v_mul_f32_e32 v11, v10, v19
	v_fma_f32 v20, -v18, v11, v10
	v_fmac_f32_e32 v11, v20, v19
	v_add_f32_e32 v13, 1.0, v13
	v_fma_f32 v10, -v18, v11, v10
	v_div_scale_f32 v18, s[8:9], v13, v13, v16
	v_rcp_f32_e32 v20, v18
	v_div_fmas_f32 v10, v10, v19, v11
	v_div_fixup_f32 v15, v10, v12, v15
	s_lshl_b64 s[8:9], s[90:91], 12
	v_fma_f32 v10, -v18, v20, 1.0
	v_fmac_f32_e32 v20, v10, v20
	v_div_scale_f32 v10, vcc, v16, v13, v16
	v_mul_f32_e32 v11, v10, v20
	v_fma_f32 v12, -v18, v11, v10
	v_fmac_f32_e32 v11, v12, v20
	v_fma_f32 v10, -v18, v11, v10
	v_div_fmas_f32 v10, v10, v20, v11
	v_div_fixup_f32 v16, v10, v13, v16
	v_pk_add_f32 v[10:11], v[38:39], v[40:41]
	s_add_u32 s8, s96, s8
	v_pk_fma_f32 v[10:11], v[10:11], s[26:27], v[42:43] op_sel_hi:[1,0,0]
	s_addc_u32 s9, s97, s9
	v_mul_f32_e32 v12, 0x4b800000, v11
	v_cmp_gt_f32_e32 vcc, s21, v11
	s_add_u32 s8, s8, s4
	s_addc_u32 s9, s9, 0
	v_cndmask_b32_e32 v11, v11, v12, vcc
	v_rsq_f32_e32 v11, v11
	v_lshl_add_u64 v[12:13], s[8:9], 0, v[92:93]
	s_lshl_b64 s[2:3], s[2:3], 12
	s_add_u32 s2, s96, s2
	v_mul_f32_e32 v18, 0x45800000, v11
	v_cndmask_b32_e32 v11, v11, v18, vcc
	v_mul_f32_e32 v6, v6, v11
	v_mul_f32_e32 v7, v7, v11
	v_mul_f32_e32 v6, v34, v6
	v_mul_f32_e32 v7, v35, v7
	v_mul_f32_e32 v6, v14, v6
	v_mul_f32_e32 v7, v17, v7
	v_cvt_pk_bf16_f32 v6, v6, v7
	v_mul_f32_e32 v7, v8, v11
	v_mul_f32_e32 v8, v9, v11
	v_mul_f32_e32 v7, v36, v7
	v_mul_f32_e32 v8, v37, v8
	v_mul_f32_e32 v7, v15, v7
	v_mul_f32_e32 v8, v16, v8
	v_cvt_pk_bf16_f32 v7, v7, v8
	v_mul_f32_e32 v8, 0x4b800000, v10
	v_cmp_gt_f32_e32 vcc, s21, v10
	s_addc_u32 s3, s97, s3
	s_add_u32 s2, s2, s4
	v_cndmask_b32_e32 v8, v10, v8, vcc
	v_rsq_f32_e32 v10, v8
	v_add_co_u32_e64 v8, s[74:75], s24, v12
	s_addc_u32 s3, s3, 0
	s_nop 0
	v_addc_co_u32_e64 v9, s[74:75], 0, v13, s[74:75]
	global_store_dwordx2 v[8:9], v[6:7], off offset:2048
	s_waitcnt vmcnt(7)
	v_lshlrev_b32_e32 v7, 16, v94
	v_mul_f32_e32 v8, 0xbfb8aa3b, v7
	v_exp_f32_e32 v8, v8
	v_mul_f32_e32 v6, 0x45800000, v10
	v_cndmask_b32_e32 v6, v10, v6, vcc
	v_and_b32_e32 v9, 0xffff0000, v94
	v_add_f32_e32 v8, 1.0, v8
	v_div_scale_f32 v11, s[8:9], v8, v8, v7
	v_rcp_f32_e32 v12, v11
	v_mul_f32_e32 v2, v2, v6
	v_mul_f32_e32 v2, v34, v2
	v_lshlrev_b32_e32 v10, 16, v95
	v_fma_f32 v14, -v11, v12, 1.0
	v_fmac_f32_e32 v12, v14, v12
	v_div_scale_f32 v14, vcc, v7, v8, v7
	v_mul_f32_e32 v15, v14, v12
	v_fma_f32 v16, -v11, v15, v14
	v_fmac_f32_e32 v15, v16, v12
	v_fma_f32 v11, -v11, v15, v14
	v_mul_f32_e32 v14, 0xbfb8aa3b, v9
	v_exp_f32_e32 v14, v14
	v_div_fmas_f32 v11, v11, v12, v15
	v_div_fixup_f32 v7, v11, v8, v7
	v_mul_f32_e32 v2, v7, v2
	v_add_f32_e32 v8, 1.0, v14
	v_div_scale_f32 v11, s[8:9], v8, v8, v9
	v_rcp_f32_e32 v12, v11
	v_mul_f32_e32 v3, v3, v6
	v_mul_f32_e32 v3, v35, v3
	v_and_b32_e32 v13, 0xffff0000, v95
	v_fma_f32 v7, -v11, v12, 1.0
	v_fmac_f32_e32 v12, v7, v12
	v_div_scale_f32 v7, vcc, v9, v8, v9
	v_mul_f32_e32 v14, v7, v12
	v_fma_f32 v15, -v11, v14, v7
	v_fmac_f32_e32 v14, v15, v12
	v_fma_f32 v7, -v11, v14, v7
	v_mul_f32_e32 v11, 0xbfb8aa3b, v10
	v_exp_f32_e32 v11, v11
	v_div_fmas_f32 v7, v7, v12, v14
	v_div_fixup_f32 v7, v7, v8, v9
	v_mul_f32_e32 v3, v7, v3
	v_add_f32_e32 v7, 1.0, v11
	v_div_scale_f32 v8, s[8:9], v7, v7, v10
	v_rcp_f32_e32 v9, v8
	v_cvt_pk_bf16_f32 v2, v2, v3
	v_mul_f32_e32 v3, v4, v6
	v_mul_f32_e32 v3, v36, v3
	v_fma_f32 v4, -v8, v9, 1.0
	v_fmac_f32_e32 v9, v4, v9
	v_div_scale_f32 v4, vcc, v10, v7, v10
	v_mul_f32_e32 v11, v4, v9
	v_fma_f32 v12, -v8, v11, v4
	v_fmac_f32_e32 v11, v12, v9
	v_fma_f32 v4, -v8, v11, v4
	v_mul_f32_e32 v8, 0xbfb8aa3b, v13
	v_exp_f32_e32 v8, v8
	v_div_fmas_f32 v4, v4, v9, v11
	v_div_fixup_f32 v4, v4, v7, v10
	v_mul_f32_e32 v3, v4, v3
	v_add_f32_e32 v7, 1.0, v8
	v_div_scale_f32 v8, s[8:9], v7, v7, v13
	v_rcp_f32_e32 v9, v8
	v_mul_f32_e32 v4, v5, v6
	v_mul_f32_e32 v4, v37, v4
	v_fma_f32 v5, -v8, v9, 1.0
	v_fmac_f32_e32 v9, v5, v9
	v_div_scale_f32 v5, vcc, v13, v7, v13
	v_mul_f32_e32 v6, v5, v9
	v_fma_f32 v10, -v8, v6, v5
	v_fmac_f32_e32 v6, v10, v9
	v_fma_f32 v5, -v8, v6, v5
	v_div_fmas_f32 v5, v5, v9, v6
	v_div_fixup_f32 v5, v5, v7, v13
	v_mul_f32_e32 v4, v5, v4
	v_cvt_pk_bf16_f32 v3, v3, v4
	v_lshl_add_u64 v[4:5], s[2:3], 0, v[92:93]
	v_add_co_u32_e32 v4, vcc, 0x55d70000, v4
	v_addc_co_u32_e32 v5, vcc, 0, v5, vcc
	s_waitcnt lgkmcnt(0)
	v_readfirstlane_b32 s28, v185
	s_lshl_b32 s36, s28, 6
	s_lshl_b32 s16, s28, 4
	s_cmpk_lt_i32 s28, 0x800
	global_store_dwordx2 v[4:5], v[2:3], off offset:2048
	s_barrier
	s_cbranch_scc0 .LBB0_1034
.LBB0_992:
	s_and_saveexec_b64 s[98:99], s[100:101]
	global_atomic_add v183, v[180:181], v182, off sc0
	s_mov_b64 exec, s[98:99]
	s_and_b32 s2, s16, 0xffffe000
	s_and_b32 s3, s36, 0x1fc0
	s_ashr_i32 s29, s28, 31
	s_bfe_u32 s10, s28, 0x20007
	s_or_b32 s25, s2, s3
	s_lshl_b64 s[2:3], s[28:29], 16
	v_readlane_b32 s0, v254, 60
	s_add_u32 s8, s0, s2
	v_readlane_b32 s0, v255, 0
	s_addc_u32 s9, s0, s3
	s_mul_i32 s3, s25, 0x2e00
	s_mul_hi_i32 s2, s25, 0x2e00
	s_add_u32 s3, s86, s3
	s_addc_u32 s11, s87, s2
	s_lshl_b32 s34, s10, 8
	s_lshl_b32 s2, s10, 9
	s_add_u32 s3, s3, s2
	s_addc_u32 s11, s11, 0
	s_add_u32 s10, s3, 0x1c00
	s_addc_u32 s11, s11, 0
	v_lshl_add_u64 v[2:3], s[10:11], 0, v[78:79]
	v_lshl_add_u64 v[2:3], v[2:3], 0, v[70:71]
	global_load_dwordx4 v[22:25], v[2:3], off
	global_load_dwordx4 v[14:17], v[2:3], off offset:256
	v_lshl_add_u64 v[2:3], s[8:9], 0, v[80:81]
	v_lshl_add_u64 v[2:3], v[2:3], 0, v[70:71]
	global_load_dwordx4 v[18:21], v[2:3], off
	global_load_dwordx4 v[6:9], v[2:3], off offset:256
	v_lshl_add_u64 v[2:3], s[8:9], 0, v[82:83]
	v_lshl_add_u64 v[26:27], s[10:11], 0, v[84:85]
	v_lshl_add_u64 v[2:3], v[2:3], 0, v[70:71]
	v_lshl_add_u64 v[26:27], v[26:27], 0, v[70:71]
	global_load_dwordx4 v[10:13], v[2:3], off
	s_nop 0
	global_load_dwordx4 v[2:5], v[2:3], off offset:256
	s_nop 0
	global_load_dwordx4 v[50:53], v[26:27], off
	global_load_dwordx4 v[46:49], v[26:27], off offset:256
	v_lshl_add_u64 v[26:27], s[8:9], 0, v[86:87]
	v_lshl_add_u64 v[26:27], v[26:27], 0, v[70:71]
	v_add_u32_e32 v56, s25, v72
	v_mov_b64_e32 v[54:55], s[86:87]
	v_add_u32_e32 v58, s25, v73
	global_load_dwordx4 v[42:45], v[26:27], off
	global_load_dwordx4 v[38:41], v[26:27], off offset:256
	v_lshl_add_u64 v[26:27], s[8:9], 0, v[88:89]
	v_mad_i64_i32 v[56:57], s[8:9], v56, s33, v[54:55]
	v_mad_i64_i32 v[54:55], s[8:9], v58, s33, v[54:55]
	v_add_u32_e32 v149, s25, v110
	v_lshl_add_u64 v[58:59], v[76:77], 0, s[34:35]
	v_mad_i64_i32 v[60:61], s[8:9], v149, s33, v[58:59]
	v_add_co_u32_e32 v60, vcc, s18, v60
	v_lshl_add_u64 v[26:27], v[26:27], 0, v[70:71]
	s_nop 0
	v_addc_co_u32_e32 v61, vcc, 0, v61, vcc
	global_load_dwordx4 v[30:33], v[26:27], off
	s_nop 0
	global_load_dwordx4 v[26:29], v[26:27], off offset:256
	s_nop 0
	global_load_ushort v148, v[60:61], off offset:1024
	global_load_ushort v147, v[60:61], off offset:2048
	v_or_b32_e32 v60, 1, v149
	v_mad_i64_i32 v[60:61], s[8:9], v60, s33, v[58:59]
	v_add_co_u32_e32 v60, vcc, s18, v60
	v_mov_b32_e32 v91, v71
	s_nop 0
	v_addc_co_u32_e32 v61, vcc, 0, v61, vcc
	global_load_ushort v109, v[60:61], off offset:1024
	global_load_ushort v108, v[60:61], off offset:2048
	v_or_b32_e32 v60, 2, v149
	v_mad_i64_i32 v[60:61], s[8:9], v60, s33, v[58:59]
	v_add_co_u32_e32 v60, vcc, s18, v60
	v_lshl_add_u64 v[56:57], v[56:57], 0, v[90:91]
	s_nop 0
	v_addc_co_u32_e32 v61, vcc, 0, v61, vcc
	global_load_ushort v106, v[60:61], off offset:1024
	global_load_ushort v104, v[60:61], off offset:2048
	v_or_b32_e32 v60, 3, v149
	v_mad_i64_i32 v[60:61], s[8:9], v60, s33, v[58:59]
	v_add_co_u32_e32 v60, vcc, s18, v60
	v_lshl_add_u64 v[54:55], v[54:55], 0, v[90:91]
	s_nop 0
	v_addc_co_u32_e32 v61, vcc, 0, v61, vcc
	global_load_ushort v107, v[60:61], off offset:1024
	global_load_ushort v105, v[60:61], off offset:2048
	v_or_b32_e32 v60, 4, v149
	v_mad_i64_i32 v[60:61], s[8:9], v60, s33, v[58:59]
	v_add_co_u32_e32 v60, vcc, s18, v60
	s_nop 1
	v_addc_co_u32_e32 v61, vcc, 0, v61, vcc
	global_load_ushort v103, v[60:61], off offset:1024
	global_load_ushort v102, v[60:61], off offset:2048
	v_or_b32_e32 v60, 5, v149
	v_mad_i64_i32 v[60:61], s[8:9], v60, s33, v[58:59]
	v_add_co_u32_e32 v60, vcc, s18, v60
	s_nop 1
	v_addc_co_u32_e32 v61, vcc, 0, v61, vcc
	global_load_ushort v101, v[60:61], off offset:1024
	global_load_ushort v100, v[60:61], off offset:2048
	v_or_b32_e32 v60, 6, v149
	v_mad_i64_i32 v[60:61], s[8:9], v60, s33, v[58:59]
	v_add_co_u32_e32 v60, vcc, s18, v60
	s_nop 1
	v_addc_co_u32_e32 v61, vcc, 0, v61, vcc
	global_load_ushort v98, v[60:61], off offset:1024
	global_load_ushort v96, v[60:61], off offset:2048
	v_or_b32_e32 v60, 7, v149
	v_mad_i64_i32 v[60:61], s[8:9], v60, s33, v[58:59]
	v_add_co_u32_e32 v60, vcc, s18, v60
	s_nop 1
	v_addc_co_u32_e32 v61, vcc, 0, v61, vcc
	global_load_ushort v99, v[60:61], off offset:1024
	global_load_ushort v97, v[60:61], off offset:2048
	v_or_b32_e32 v60, 8, v149
	v_mad_i64_i32 v[60:61], s[8:9], v60, s33, v[58:59]
	v_add_co_u32_e32 v60, vcc, s18, v60
	s_nop 1
	v_addc_co_u32_e32 v61, vcc, 0, v61, vcc
	global_load_ushort v95, v[60:61], off offset:1024
	global_load_ushort v94, v[60:61], off offset:2048
	v_or_b32_e32 v60, 9, v149
	v_mad_i64_i32 v[60:61], s[8:9], v60, s33, v[58:59]
	v_add_co_u32_e32 v60, vcc, s18, v60
	s_nop 1
	v_addc_co_u32_e32 v61, vcc, 0, v61, vcc
	global_load_ushort v93, v[60:61], off offset:1024
	global_load_ushort v91, v[60:61], off offset:2048
	v_or_b32_e32 v60, 10, v149
	v_mad_i64_i32 v[60:61], s[8:9], v60, s33, v[58:59]
	v_add_co_u32_e32 v60, vcc, s18, v60
	s_nop 1
	v_addc_co_u32_e32 v61, vcc, 0, v61, vcc
	global_load_ushort v68, v[60:61], off offset:1024
	global_load_ushort v66, v[60:61], off offset:2048
	v_or_b32_e32 v60, 11, v149
	v_mad_i64_i32 v[60:61], s[8:9], v60, s33, v[58:59]
	v_add_co_u32_e32 v60, vcc, s18, v60
	s_nop 1
	v_addc_co_u32_e32 v61, vcc, 0, v61, vcc
	global_load_ushort v69, v[60:61], off offset:1024
	global_load_ushort v67, v[60:61], off offset:2048
	v_or_b32_e32 v60, 12, v149
	v_mad_i64_i32 v[60:61], s[8:9], v60, s33, v[58:59]
	v_add_co_u32_e32 v60, vcc, s18, v60
	s_nop 1
	v_addc_co_u32_e32 v61, vcc, 0, v61, vcc
	global_load_ushort v65, v[60:61], off offset:1024
	global_load_ushort v64, v[60:61], off offset:2048
	v_or_b32_e32 v60, 13, v149
	v_mad_i64_i32 v[60:61], s[8:9], v60, s33, v[58:59]
	v_add_co_u32_e32 v60, vcc, s18, v60
	s_nop 1
	v_addc_co_u32_e32 v61, vcc, 0, v61, vcc
	global_load_ushort v63, v[60:61], off offset:1024
	global_load_ushort v62, v[60:61], off offset:2048
	v_or_b32_e32 v60, 14, v149
	v_mad_i64_i32 v[60:61], s[8:9], v60, s33, v[58:59]
	v_add_co_u32_e32 v150, vcc, s18, v60
	v_or_b32_e32 v149, 15, v149
	s_nop 0
	v_addc_co_u32_e32 v151, vcc, 0, v61, vcc
	v_mad_i64_i32 v[58:59], s[8:9], v149, s33, v[58:59]
	global_load_ushort v61, v[150:151], off offset:1024
	global_load_ushort v60, v[150:151], off offset:2048
	v_add_co_u32_e32 v150, vcc, s18, v58
	s_nop 1
	v_addc_co_u32_e32 v151, vcc, 0, v59, vcc
	global_load_ushort v59, v[150:151], off offset:1024
	global_load_ushort v58, v[150:151], off offset:2048
	v_lshl_or_b32 v150, v1, 2, s2
	v_readlane_b32 s0, v254, 27
	v_mov_b32_e32 v151, v71
	v_readlane_b32 s10, v254, 37
	v_readlane_b32 s11, v254, 38
	v_readlane_b32 s12, v254, 39
	v_readlane_b32 s13, v254, 40
	v_lshl_add_u64 v[152:153], s[10:11], 0, v[150:151]
	v_readlane_b32 s2, v254, 29
	s_movk_i32 s2, 0x3000
	v_readlane_b32 s3, v254, 30
	v_readlane_b32 s1, v254, 28
	global_load_dword v149, v150, s[12:13]
	global_load_dword v162, v150, s[10:11]
	global_load_dword v163, v150, s[10:11] offset:2048
	v_add_co_u32_e32 v150, vcc, s18, v152
	v_readlane_b32 s4, v254, 31
	s_nop 0
	v_addc_co_u32_e32 v151, vcc, 0, v153, vcc
	v_add_co_u32_e32 v154, vcc, s19, v152
	v_readlane_b32 s5, v254, 32
	s_nop 0
	v_addc_co_u32_e32 v155, vcc, 0, v153, vcc
	global_load_dword v164, v[154:155], off offset:-4096
	global_load_dword v165, v[150:151], off offset:2048
	global_load_dword v156, v[154:155], off
	global_load_dword v157, v[154:155], off offset:2048
	v_add_co_u32_e32 v150, vcc, s2, v152
	s_movk_i32 s2, 0x4000
	s_nop 0
	v_addc_co_u32_e32 v151, vcc, 0, v153, vcc
	v_add_co_u32_e32 v158, vcc, s2, v152
	s_movk_i32 s2, 0x5000
	s_nop 0
	v_addc_co_u32_e32 v159, vcc, 0, v153, vcc
	global_load_dword v160, v[158:159], off offset:-4096
	global_load_dword v161, v[150:151], off offset:2048
	global_load_dword v154, v[158:159], off
	global_load_dword v155, v[158:159], off offset:2048
	v_add_co_u32_e32 v150, vcc, s2, v152
	s_movk_i32 s2, 0x6000
	s_nop 0
	v_addc_co_u32_e32 v151, vcc, 0, v153, vcc
	v_add_co_u32_e32 v166, vcc, s2, v152
	s_movk_i32 s2, 0x7000
	s_nop 0
	v_addc_co_u32_e32 v167, vcc, 0, v153, vcc
	global_load_dword v158, v[166:167], off offset:-4096
	global_load_dword v159, v[150:151], off offset:2048
	s_nop 0
	global_load_dword v151, v[166:167], off
	global_load_dword v150, v[166:167], off offset:2048
	v_add_co_u32_e32 v166, vcc, s2, v152
	s_mov_b32 s2, 0x3d800000
	s_nop 0
	v_addc_co_u32_e32 v167, vcc, 0, v153, vcc
	v_add_co_u32_e32 v56, vcc, s19, v56
	global_load_dword v153, v[166:167], off
	global_load_dword v152, v[166:167], off offset:2048
	v_addc_co_u32_e32 v57, vcc, 0, v57, vcc
	v_add_co_u32_e32 v54, vcc, s19, v54
	global_load_ushort v56, v[56:57], off offset:3120
	s_nop 0
	v_addc_co_u32_e32 v55, vcc, 0, v55, vcc
	global_load_ushort v54, v[54:55], off offset:3120
	v_add_u32_e32 v166, v75, v116
	s_waitcnt vmcnt(62)
	ds_write_b128 v166, v[22:25] offset:40960
	v_add_u32_e32 v22, v75, v117
	s_waitcnt vmcnt(56)
	ds_write_b128 v22, v[50:53] offset:40960
	ds_write_b128 v166, v[14:17] offset:57344
	s_waitcnt vmcnt(55)
	ds_write_b128 v22, v[46:49] offset:57344
	v_add_u32_e32 v14, v111, v116
	v_add_u32_e32 v15, v111, v117
	ds_write_b128 v14, v[18:21] offset:32768
	s_waitcnt vmcnt(54)
	ds_write_b128 v15, v[42:45] offset:32768
	ds_write_b128 v14, v[6:9] offset:49152
	s_waitcnt vmcnt(53)
	ds_write_b128 v15, v[38:41] offset:49152
	v_add_u32_e32 v6, v118, v116
	ds_write_b128 v6, v[10:13]
	v_add_u32_e32 v6, v118, v117
	s_waitcnt vmcnt(52)
	ds_write_b128 v6, v[30:33]
	v_add_u32_e32 v6, v119, v116
	ds_write_b128 v6, v[2:5]
	v_add_u32_e32 v2, v119, v117
	s_waitcnt vmcnt(51)
	ds_write_b128 v2, v[26:29]
	v_readlane_b32 s6, v254, 33
	v_readlane_b32 s7, v254, 34
	v_readlane_b32 s8, v254, 35
	v_readlane_b32 s9, v254, 36
	v_readlane_b32 s14, v254, 41
	v_readlane_b32 s15, v254, 42
	s_waitcnt vmcnt(1)
	v_lshlrev_b32_e32 v2, 16, v56
	s_waitcnt vmcnt(0)
	v_lshlrev_b32_e32 v3, 16, v54
	ds_write2st64_b32 v112, v2, v3 offset0:144 offset1:152
	s_and_saveexec_b64 s[98:99], s[100:101]
	ds_write_b32 v184, v183
	s_mov_b64 exec, s[98:99]
	v_mov_b32_e32 v2, v0
	s_waitcnt lgkmcnt(0)
	s_barrier
	ds_read_b32 v185, v184
	s_nop 0
	v_ashrrev_i32_e32 v4, 7, v2
	v_lshl_add_u32 v3, v4, 10, 0
	ds_read_b128 v[6:9], v3 offset:36864
	ds_read_b128 v[10:13], v3 offset:36880
	ds_read_b128 v[14:17], v3 offset:36896
	ds_read_b128 v[18:21], v3 offset:36912
	s_waitcnt lgkmcnt(3)
	v_fma_f32 v5, v6, v162, v149
	v_fmac_f32_e32 v5, v7, v163
	v_fmac_f32_e32 v5, v8, v164
	v_fmac_f32_e32 v5, v9, v165
	s_waitcnt lgkmcnt(2)
	v_fmac_f32_e32 v5, v10, v156
	v_fmac_f32_e32 v5, v11, v157
	v_fmac_f32_e32 v5, v12, v160
	v_fmac_f32_e32 v5, v13, v161
	s_waitcnt lgkmcnt(1)
	v_fmac_f32_e32 v5, v14, v154
	v_fmac_f32_e32 v5, v15, v155
	v_fmac_f32_e32 v5, v16, v158
	v_fmac_f32_e32 v5, v17, v159
	s_waitcnt lgkmcnt(0)
	v_fmac_f32_e32 v5, v18, v151
	v_fmac_f32_e32 v5, v19, v150
	v_fmac_f32_e32 v5, v20, v153
	v_fmac_f32_e32 v5, v21, v152
	v_min_f32_e32 v6, 0, v5
	v_mul_f32_e64 v5, |v5|, s20
	v_exp_f32_e32 v5, v5
	s_nop 0
	v_add_f32_e32 v5, 1.0, v5
	v_cmp_gt_f32_e32 vcc, s21, v5
	s_nop 1
	v_cndmask_b32_e64 v7, 0, 32, vcc
	v_ldexp_f32 v5, v5, v7
	v_log_f32_e32 v5, v5
	s_nop 0
	v_mul_f32_e32 v7, 0x3f317217, v5
	v_fma_f32 v7, v5, s22, -v7
	v_fmac_f32_e32 v7, 0x3377d1cf, v5
	v_fmac_f32_e32 v7, 0x3f317217, v5
	v_cmp_lt_f32_e64 s[74:75], |v5|, s23
	s_nop 1
	v_cndmask_b32_e64 v5, v5, v7, s[74:75]
	v_cndmask_b32_e32 v7, 0, v145, vcc
	v_sub_f32_e32 v5, v5, v7
	v_sub_f32_e32 v5, v6, v5
	ds_read_b128 v[6:9], v3 offset:36928
	v_fma_f32 v5, v5, s2, 0
	s_movk_i32 s2, 0x7f
	s_waitcnt lgkmcnt(0)
	v_fma_f32 v10, v6, v162, v149
	v_fmac_f32_e32 v10, v7, v163
	v_fmac_f32_e32 v10, v8, v164
	v_fmac_f32_e32 v10, v9, v165
	ds_read_b128 v[6:9], v3 offset:36944
	s_waitcnt lgkmcnt(0)
	v_fmac_f32_e32 v10, v6, v156
	v_fmac_f32_e32 v10, v7, v157
	v_fmac_f32_e32 v10, v8, v160
	v_fmac_f32_e32 v10, v9, v161
	ds_read_b128 v[6:9], v3 offset:36960
	s_waitcnt lgkmcnt(0)
	v_fmac_f32_e32 v10, v6, v154
	v_fmac_f32_e32 v10, v7, v155
	v_fmac_f32_e32 v10, v8, v158
	v_fmac_f32_e32 v10, v9, v159
	ds_read_b128 v[6:9], v3 offset:36976
	s_waitcnt lgkmcnt(0)
	v_fmac_f32_e32 v10, v6, v151
	v_fmac_f32_e32 v10, v7, v150
	v_fmac_f32_e32 v10, v8, v153
	v_fmac_f32_e32 v10, v9, v152
	v_mul_f32_e64 v7, |v10|, s20
	v_exp_f32_e32 v7, v7
	v_min_f32_e32 v6, 0, v10
	v_add_f32_e32 v7, 1.0, v7
	v_cmp_gt_f32_e32 vcc, s21, v7
	s_nop 1
	v_cndmask_b32_e64 v8, 0, 32, vcc
	v_ldexp_f32 v7, v7, v8
	v_log_f32_e32 v7, v7
	s_nop 0
	v_mul_f32_e32 v8, 0x3f317217, v7
	v_fma_f32 v8, v7, s22, -v8
	v_fmac_f32_e32 v8, 0x3377d1cf, v7
	v_fmac_f32_e32 v8, 0x3f317217, v7
	v_cmp_lt_f32_e64 s[74:75], |v7|, s23
	s_nop 1
	v_cndmask_b32_e64 v7, v7, v8, s[74:75]
	v_cndmask_b32_e32 v8, 0, v145, vcc
	v_sub_f32_e32 v7, v7, v8
	ds_read_b128 v[8:11], v3 offset:36992
	v_sub_f32_e32 v6, v6, v7
	v_fmamk_f32 v6, v6, 0x3d800000, v5
	s_waitcnt lgkmcnt(0)
	v_fma_f32 v7, v8, v162, v149
	v_fmac_f32_e32 v7, v9, v163
	v_fmac_f32_e32 v7, v10, v164
	v_fmac_f32_e32 v7, v11, v165
	ds_read_b128 v[8:11], v3 offset:37008
	s_waitcnt lgkmcnt(0)
	v_fmac_f32_e32 v7, v8, v156
	v_fmac_f32_e32 v7, v9, v157
	v_fmac_f32_e32 v7, v10, v160
	v_fmac_f32_e32 v7, v11, v161
	ds_read_b128 v[8:11], v3 offset:37024
	s_waitcnt lgkmcnt(0)
	v_fmac_f32_e32 v7, v8, v154
	v_fmac_f32_e32 v7, v9, v155
	v_fmac_f32_e32 v7, v10, v158
	v_fmac_f32_e32 v7, v11, v159
	ds_read_b128 v[8:11], v3 offset:37040
	s_waitcnt lgkmcnt(0)
	v_fmac_f32_e32 v7, v8, v151
	v_fmac_f32_e32 v7, v9, v150
	v_fmac_f32_e32 v7, v10, v153
	v_fmac_f32_e32 v7, v11, v152
	v_min_f32_e32 v8, 0, v7
	v_mul_f32_e64 v7, |v7|, s20
	v_exp_f32_e32 v7, v7
	s_nop 0
	v_add_f32_e32 v7, 1.0, v7
	v_cmp_gt_f32_e32 vcc, s21, v7
	s_nop 1
	v_cndmask_b32_e64 v9, 0, 32, vcc
	v_ldexp_f32 v7, v7, v9
	v_log_f32_e32 v7, v7
	s_nop 0
	v_mul_f32_e32 v9, 0x3f317217, v7
	v_fma_f32 v9, v7, s22, -v9
	v_fmac_f32_e32 v9, 0x3377d1cf, v7
	v_fmac_f32_e32 v9, 0x3f317217, v7
	v_cmp_lt_f32_e64 s[74:75], |v7|, s23
	s_nop 1
	v_cndmask_b32_e64 v7, v7, v9, s[74:75]
	v_cndmask_b32_e32 v9, 0, v145, vcc
	v_sub_f32_e32 v7, v7, v9
	v_sub_f32_e32 v7, v8, v7
	ds_read_b128 v[8:11], v3 offset:37056
	v_fmamk_f32 v7, v7, 0x3d800000, v6
	s_waitcnt lgkmcnt(0)
	v_fma_f32 v12, v8, v162, v149
	v_fmac_f32_e32 v12, v9, v163
	v_fmac_f32_e32 v12, v10, v164
	v_fmac_f32_e32 v12, v11, v165
	ds_read_b128 v[8:11], v3 offset:37072
	s_waitcnt lgkmcnt(0)
	v_fmac_f32_e32 v12, v8, v156
	v_fmac_f32_e32 v12, v9, v157
	v_fmac_f32_e32 v12, v10, v160
	v_fmac_f32_e32 v12, v11, v161
	ds_read_b128 v[8:11], v3 offset:37088
	s_waitcnt lgkmcnt(0)
	v_fmac_f32_e32 v12, v8, v154
	v_fmac_f32_e32 v12, v9, v155
	v_fmac_f32_e32 v12, v10, v158
	v_fmac_f32_e32 v12, v11, v159
	ds_read_b128 v[8:11], v3 offset:37104
	s_waitcnt lgkmcnt(0)
	v_fmac_f32_e32 v12, v8, v151
	v_fmac_f32_e32 v12, v9, v150
	v_fmac_f32_e32 v12, v10, v153
	v_fmac_f32_e32 v12, v11, v152
	v_mul_f32_e64 v9, |v12|, s20
	v_exp_f32_e32 v9, v9
	v_min_f32_e32 v8, 0, v12
	v_add_f32_e32 v9, 1.0, v9
	v_cmp_gt_f32_e32 vcc, s21, v9
	s_nop 1
	v_cndmask_b32_e64 v10, 0, 32, vcc
	v_ldexp_f32 v9, v9, v10
	v_log_f32_e32 v9, v9
	s_nop 0
	v_mul_f32_e32 v10, 0x3f317217, v9
	v_fma_f32 v10, v9, s22, -v10
	v_fmac_f32_e32 v10, 0x3377d1cf, v9
	v_fmac_f32_e32 v10, 0x3f317217, v9
	v_cmp_lt_f32_e64 s[74:75], |v9|, s23
	s_nop 1
	v_cndmask_b32_e64 v9, v9, v10, s[74:75]
	v_cndmask_b32_e32 v10, 0, v145, vcc
	v_sub_f32_e32 v9, v9, v10
	ds_read_b128 v[10:13], v3 offset:37120
	v_sub_f32_e32 v8, v8, v9
	v_fmamk_f32 v8, v8, 0x3d800000, v7
	s_waitcnt lgkmcnt(0)
	v_fma_f32 v9, v10, v162, v149
	v_fmac_f32_e32 v9, v11, v163
	v_fmac_f32_e32 v9, v12, v164
	v_fmac_f32_e32 v9, v13, v165
	ds_read_b128 v[10:13], v3 offset:37136
	s_waitcnt lgkmcnt(0)
	v_fmac_f32_e32 v9, v10, v156
	v_fmac_f32_e32 v9, v11, v157
	v_fmac_f32_e32 v9, v12, v160
	v_fmac_f32_e32 v9, v13, v161
	ds_read_b128 v[10:13], v3 offset:37152
	s_waitcnt lgkmcnt(0)
	v_fmac_f32_e32 v9, v10, v154
	v_fmac_f32_e32 v9, v11, v155
	v_fmac_f32_e32 v9, v12, v158
	v_fmac_f32_e32 v9, v13, v159
	ds_read_b128 v[10:13], v3 offset:37168
	s_waitcnt lgkmcnt(0)
	v_fmac_f32_e32 v9, v10, v151
	v_fmac_f32_e32 v9, v11, v150
	v_fmac_f32_e32 v9, v12, v153
	v_fmac_f32_e32 v9, v13, v152
	v_min_f32_e32 v10, 0, v9
	v_mul_f32_e64 v9, |v9|, s20
	v_exp_f32_e32 v9, v9
	s_nop 0
	v_add_f32_e32 v9, 1.0, v9
	v_cmp_gt_f32_e32 vcc, s21, v9
	s_nop 1
	v_cndmask_b32_e64 v11, 0, 32, vcc
	v_ldexp_f32 v9, v9, v11
	v_log_f32_e32 v9, v9
	s_nop 0
	v_mul_f32_e32 v11, 0x3f317217, v9
	v_fma_f32 v11, v9, s22, -v11
	v_fmac_f32_e32 v11, 0x3377d1cf, v9
	v_fmac_f32_e32 v11, 0x3f317217, v9
	v_cmp_lt_f32_e64 s[74:75], |v9|, s23
	s_nop 1
	v_cndmask_b32_e64 v9, v9, v11, s[74:75]
	v_cndmask_b32_e32 v11, 0, v145, vcc
	v_sub_f32_e32 v9, v9, v11
	v_sub_f32_e32 v9, v10, v9
	ds_read_b128 v[10:13], v3 offset:37184
	v_fmamk_f32 v9, v9, 0x3d800000, v8
	s_waitcnt lgkmcnt(0)
	v_fma_f32 v14, v10, v162, v149
	v_fmac_f32_e32 v14, v11, v163
	v_fmac_f32_e32 v14, v12, v164
	v_fmac_f32_e32 v14, v13, v165
	ds_read_b128 v[10:13], v3 offset:37200
	s_waitcnt lgkmcnt(0)
	v_fmac_f32_e32 v14, v10, v156
	v_fmac_f32_e32 v14, v11, v157
	v_fmac_f32_e32 v14, v12, v160
	v_fmac_f32_e32 v14, v13, v161
	ds_read_b128 v[10:13], v3 offset:37216
	s_waitcnt lgkmcnt(0)
	v_fmac_f32_e32 v14, v10, v154
	v_fmac_f32_e32 v14, v11, v155
	v_fmac_f32_e32 v14, v12, v158
	v_fmac_f32_e32 v14, v13, v159
	ds_read_b128 v[10:13], v3 offset:37232
	s_waitcnt lgkmcnt(0)
	v_fmac_f32_e32 v14, v10, v151
	v_fmac_f32_e32 v14, v11, v150
	v_fmac_f32_e32 v14, v12, v153
	v_fmac_f32_e32 v14, v13, v152
	v_mul_f32_e64 v11, |v14|, s20
	v_exp_f32_e32 v11, v11
	v_min_f32_e32 v10, 0, v14
	v_add_f32_e32 v11, 1.0, v11
	v_cmp_gt_f32_e32 vcc, s21, v11
	s_nop 1
	v_cndmask_b32_e64 v12, 0, 32, vcc
	v_ldexp_f32 v11, v11, v12
	v_log_f32_e32 v11, v11
	s_nop 0
	v_mul_f32_e32 v12, 0x3f317217, v11
	v_fma_f32 v12, v11, s22, -v12
	v_fmac_f32_e32 v12, 0x3377d1cf, v11
	v_fmac_f32_e32 v12, 0x3f317217, v11
	v_cmp_lt_f32_e64 s[74:75], |v11|, s23
	s_nop 1
	v_cndmask_b32_e64 v11, v11, v12, s[74:75]
	v_cndmask_b32_e32 v12, 0, v145, vcc
	v_sub_f32_e32 v11, v11, v12
	ds_read_b128 v[12:15], v3 offset:37248
	v_sub_f32_e32 v10, v10, v11
	v_fmamk_f32 v10, v10, 0x3d800000, v9
	s_waitcnt lgkmcnt(0)
	v_fma_f32 v11, v12, v162, v149
	v_fmac_f32_e32 v11, v13, v163
	v_fmac_f32_e32 v11, v14, v164
	v_fmac_f32_e32 v11, v15, v165
	ds_read_b128 v[12:15], v3 offset:37264
	s_waitcnt lgkmcnt(0)
	v_fmac_f32_e32 v11, v12, v156
	v_fmac_f32_e32 v11, v13, v157
	v_fmac_f32_e32 v11, v14, v160
	v_fmac_f32_e32 v11, v15, v161
	ds_read_b128 v[12:15], v3 offset:37280
	s_waitcnt lgkmcnt(0)
	v_fmac_f32_e32 v11, v12, v154
	v_fmac_f32_e32 v11, v13, v155
	v_fmac_f32_e32 v11, v14, v158
	v_fmac_f32_e32 v11, v15, v159
	ds_read_b128 v[12:15], v3 offset:37296
	s_waitcnt lgkmcnt(0)
	v_fmac_f32_e32 v11, v12, v151
	v_fmac_f32_e32 v11, v13, v150
	v_fmac_f32_e32 v11, v14, v153
	v_fmac_f32_e32 v11, v15, v152
	v_min_f32_e32 v12, 0, v11
	v_mul_f32_e64 v11, |v11|, s20
	v_exp_f32_e32 v11, v11
	s_nop 0
	v_add_f32_e32 v11, 1.0, v11
	v_cmp_gt_f32_e32 vcc, s21, v11
	s_nop 1
	v_cndmask_b32_e64 v13, 0, 32, vcc
	v_ldexp_f32 v11, v11, v13
	v_log_f32_e32 v11, v11
	s_nop 0
	v_mul_f32_e32 v13, 0x3f317217, v11
	v_fma_f32 v13, v11, s22, -v13
	v_fmac_f32_e32 v13, 0x3377d1cf, v11
	v_fmac_f32_e32 v13, 0x3f317217, v11
	v_cmp_lt_f32_e64 s[74:75], |v11|, s23
	s_nop 1
	v_cndmask_b32_e64 v11, v11, v13, s[74:75]
	v_cndmask_b32_e32 v13, 0, v145, vcc
	v_sub_f32_e32 v11, v11, v13
	v_sub_f32_e32 v11, v12, v11
	ds_read_b128 v[12:15], v3 offset:37312
	v_fmamk_f32 v11, v11, 0x3d800000, v10
	s_waitcnt lgkmcnt(0)
	v_fma_f32 v16, v12, v162, v149
	v_fmac_f32_e32 v16, v13, v163
	v_fmac_f32_e32 v16, v14, v164
	v_fmac_f32_e32 v16, v15, v165
	ds_read_b128 v[12:15], v3 offset:37328
	s_waitcnt lgkmcnt(0)
	v_fmac_f32_e32 v16, v12, v156
	v_fmac_f32_e32 v16, v13, v157
	v_fmac_f32_e32 v16, v14, v160
	v_fmac_f32_e32 v16, v15, v161
	ds_read_b128 v[12:15], v3 offset:37344
	s_waitcnt lgkmcnt(0)
	v_fmac_f32_e32 v16, v12, v154
	v_fmac_f32_e32 v16, v13, v155
	v_fmac_f32_e32 v16, v14, v158
	v_fmac_f32_e32 v16, v15, v159
	ds_read_b128 v[12:15], v3 offset:37360
	s_waitcnt lgkmcnt(0)
	v_fmac_f32_e32 v16, v12, v151
	v_fmac_f32_e32 v16, v13, v150
	v_fmac_f32_e32 v16, v14, v153
	v_fmac_f32_e32 v16, v15, v152
	v_mul_f32_e64 v13, |v16|, s20
	v_exp_f32_e32 v13, v13
	v_min_f32_e32 v12, 0, v16
	v_add_f32_e32 v13, 1.0, v13
	v_cmp_gt_f32_e32 vcc, s21, v13
	s_nop 1
	v_cndmask_b32_e64 v14, 0, 32, vcc
	v_ldexp_f32 v13, v13, v14
	v_log_f32_e32 v13, v13
	s_nop 0
	v_mul_f32_e32 v14, 0x3f317217, v13
	v_fma_f32 v14, v13, s22, -v14
	v_fmac_f32_e32 v14, 0x3377d1cf, v13
	v_fmac_f32_e32 v14, 0x3f317217, v13
	v_cmp_lt_f32_e64 s[74:75], |v13|, s23
	s_nop 1
	v_cndmask_b32_e64 v13, v13, v14, s[74:75]
	v_cndmask_b32_e32 v14, 0, v145, vcc
	v_sub_f32_e32 v13, v13, v14
	ds_read_b128 v[14:17], v3 offset:37376
	v_sub_f32_e32 v12, v12, v13
	v_fmamk_f32 v12, v12, 0x3d800000, v11
	s_waitcnt lgkmcnt(0)
	v_fma_f32 v13, v14, v162, v149
	v_fmac_f32_e32 v13, v15, v163
	v_fmac_f32_e32 v13, v16, v164
	v_fmac_f32_e32 v13, v17, v165
	ds_read_b128 v[14:17], v3 offset:37392
	s_waitcnt lgkmcnt(0)
	v_fmac_f32_e32 v13, v14, v156
	v_fmac_f32_e32 v13, v15, v157
	v_fmac_f32_e32 v13, v16, v160
	v_fmac_f32_e32 v13, v17, v161
	ds_read_b128 v[14:17], v3 offset:37408
	s_waitcnt lgkmcnt(0)
	v_fmac_f32_e32 v13, v14, v154
	v_fmac_f32_e32 v13, v15, v155
	v_fmac_f32_e32 v13, v16, v158
	v_fmac_f32_e32 v13, v17, v159
	ds_read_b128 v[14:17], v3 offset:37424
	s_waitcnt lgkmcnt(0)
	v_fmac_f32_e32 v13, v14, v151
	v_fmac_f32_e32 v13, v15, v150
	v_fmac_f32_e32 v13, v16, v153
	v_fmac_f32_e32 v13, v17, v152
	v_min_f32_e32 v14, 0, v13
	v_mul_f32_e64 v13, |v13|, s20
	v_exp_f32_e32 v13, v13
	s_nop 0
	v_add_f32_e32 v13, 1.0, v13
	v_cmp_gt_f32_e32 vcc, s21, v13
	s_nop 1
	v_cndmask_b32_e64 v15, 0, 32, vcc
	v_ldexp_f32 v13, v13, v15
	v_log_f32_e32 v13, v13
	s_nop 0
	v_mul_f32_e32 v15, 0x3f317217, v13
	v_fma_f32 v15, v13, s22, -v15
	v_fmac_f32_e32 v15, 0x3377d1cf, v13
	v_fmac_f32_e32 v15, 0x3f317217, v13
	v_cmp_lt_f32_e64 s[74:75], |v13|, s23
	s_nop 1
	v_cndmask_b32_e64 v13, v13, v15, s[74:75]
	v_cndmask_b32_e32 v15, 0, v145, vcc
	v_sub_f32_e32 v13, v13, v15
	v_sub_f32_e32 v13, v14, v13
	ds_read_b128 v[14:17], v3 offset:37440
	v_fmamk_f32 v13, v13, 0x3d800000, v12
	s_waitcnt lgkmcnt(0)
	v_fma_f32 v18, v14, v162, v149
	v_fmac_f32_e32 v18, v15, v163
	v_fmac_f32_e32 v18, v16, v164
	v_fmac_f32_e32 v18, v17, v165
	ds_read_b128 v[14:17], v3 offset:37456
	s_waitcnt lgkmcnt(0)
	v_fmac_f32_e32 v18, v14, v156
	v_fmac_f32_e32 v18, v15, v157
	v_fmac_f32_e32 v18, v16, v160
	v_fmac_f32_e32 v18, v17, v161
	ds_read_b128 v[14:17], v3 offset:37472
	s_waitcnt lgkmcnt(0)
	v_fmac_f32_e32 v18, v14, v154
	v_fmac_f32_e32 v18, v15, v155
	v_fmac_f32_e32 v18, v16, v158
	v_fmac_f32_e32 v18, v17, v159
	ds_read_b128 v[14:17], v3 offset:37488
	s_waitcnt lgkmcnt(0)
	v_fmac_f32_e32 v18, v14, v151
	v_fmac_f32_e32 v18, v15, v150
	v_fmac_f32_e32 v18, v16, v153
	v_fmac_f32_e32 v18, v17, v152
	v_mul_f32_e64 v15, |v18|, s20
	v_exp_f32_e32 v15, v15
	v_min_f32_e32 v14, 0, v18
	v_add_f32_e32 v15, 1.0, v15
	v_cmp_gt_f32_e32 vcc, s21, v15
	s_nop 1
	v_cndmask_b32_e64 v16, 0, 32, vcc
	v_ldexp_f32 v15, v15, v16
	v_log_f32_e32 v15, v15
	s_nop 0
	v_mul_f32_e32 v16, 0x3f317217, v15
	v_fma_f32 v16, v15, s22, -v16
	v_fmac_f32_e32 v16, 0x3377d1cf, v15
	v_fmac_f32_e32 v16, 0x3f317217, v15
	v_cmp_lt_f32_e64 s[74:75], |v15|, s23
	s_nop 1
	v_cndmask_b32_e64 v15, v15, v16, s[74:75]
	v_cndmask_b32_e32 v16, 0, v145, vcc
	v_sub_f32_e32 v15, v15, v16
	ds_read_b128 v[16:19], v3 offset:37504
	v_sub_f32_e32 v14, v14, v15
	v_fmamk_f32 v14, v14, 0x3d800000, v13
	s_waitcnt lgkmcnt(0)
	v_fma_f32 v15, v16, v162, v149
	v_fmac_f32_e32 v15, v17, v163
	v_fmac_f32_e32 v15, v18, v164
	v_fmac_f32_e32 v15, v19, v165
	ds_read_b128 v[16:19], v3 offset:37520
	s_waitcnt lgkmcnt(0)
	v_fmac_f32_e32 v15, v16, v156
	v_fmac_f32_e32 v15, v17, v157
	v_fmac_f32_e32 v15, v18, v160
	v_fmac_f32_e32 v15, v19, v161
	ds_read_b128 v[16:19], v3 offset:37536
	s_waitcnt lgkmcnt(0)
	v_fmac_f32_e32 v15, v16, v154
	v_fmac_f32_e32 v15, v17, v155
	v_fmac_f32_e32 v15, v18, v158
	v_fmac_f32_e32 v15, v19, v159
	ds_read_b128 v[16:19], v3 offset:37552
	s_waitcnt lgkmcnt(0)
	v_fmac_f32_e32 v15, v16, v151
	v_fmac_f32_e32 v15, v17, v150
	v_fmac_f32_e32 v15, v18, v153
	v_fmac_f32_e32 v15, v19, v152
	v_min_f32_e32 v16, 0, v15
	v_mul_f32_e64 v15, |v15|, s20
	v_exp_f32_e32 v15, v15
	s_nop 0
	v_add_f32_e32 v15, 1.0, v15
	v_cmp_gt_f32_e32 vcc, s21, v15
	s_nop 1
	v_cndmask_b32_e64 v17, 0, 32, vcc
	v_ldexp_f32 v15, v15, v17
	v_log_f32_e32 v15, v15
	s_nop 0
	v_mul_f32_e32 v17, 0x3f317217, v15
	v_fma_f32 v17, v15, s22, -v17
	v_fmac_f32_e32 v17, 0x3377d1cf, v15
	v_fmac_f32_e32 v17, 0x3f317217, v15
	v_cmp_lt_f32_e64 s[74:75], |v15|, s23
	s_nop 1
	v_cndmask_b32_e64 v15, v15, v17, s[74:75]
	v_cndmask_b32_e32 v17, 0, v145, vcc
	v_sub_f32_e32 v15, v15, v17
	v_sub_f32_e32 v15, v16, v15
	ds_read_b128 v[16:19], v3 offset:37568
	v_fmamk_f32 v15, v15, 0x3d800000, v14
	s_waitcnt lgkmcnt(0)
	v_fma_f32 v20, v16, v162, v149
	v_fmac_f32_e32 v20, v17, v163
	v_fmac_f32_e32 v20, v18, v164
	v_fmac_f32_e32 v20, v19, v165
	ds_read_b128 v[16:19], v3 offset:37584
	s_waitcnt lgkmcnt(0)
	v_fmac_f32_e32 v20, v16, v156
	v_fmac_f32_e32 v20, v17, v157
	v_fmac_f32_e32 v20, v18, v160
	v_fmac_f32_e32 v20, v19, v161
	ds_read_b128 v[16:19], v3 offset:37600
	s_waitcnt lgkmcnt(0)
	v_fmac_f32_e32 v20, v16, v154
	v_fmac_f32_e32 v20, v17, v155
	v_fmac_f32_e32 v20, v18, v158
	v_fmac_f32_e32 v20, v19, v159
	ds_read_b128 v[16:19], v3 offset:37616
	s_waitcnt lgkmcnt(0)
	v_fmac_f32_e32 v20, v16, v151
	v_fmac_f32_e32 v20, v17, v150
	v_fmac_f32_e32 v20, v18, v153
	v_fmac_f32_e32 v20, v19, v152
	v_mul_f32_e64 v17, |v20|, s20
	v_exp_f32_e32 v17, v17
	v_min_f32_e32 v16, 0, v20
	v_add_f32_e32 v17, 1.0, v17
	v_cmp_gt_f32_e32 vcc, s21, v17
	s_nop 1
	v_cndmask_b32_e64 v18, 0, 32, vcc
	v_ldexp_f32 v17, v17, v18
	v_log_f32_e32 v17, v17
	s_nop 0
	v_mul_f32_e32 v18, 0x3f317217, v17
	v_fma_f32 v18, v17, s22, -v18
	v_fmac_f32_e32 v18, 0x3377d1cf, v17
	v_fmac_f32_e32 v18, 0x3f317217, v17
	v_cmp_lt_f32_e64 s[74:75], |v17|, s23
	s_nop 1
	v_cndmask_b32_e64 v17, v17, v18, s[74:75]
	v_cndmask_b32_e32 v18, 0, v145, vcc
	v_sub_f32_e32 v17, v17, v18
	ds_read_b128 v[18:21], v3 offset:37632
	v_sub_f32_e32 v16, v16, v17
	v_fmamk_f32 v16, v16, 0x3d800000, v15
	s_waitcnt lgkmcnt(0)
	v_fma_f32 v17, v18, v162, v149
	v_fmac_f32_e32 v17, v19, v163
	v_fmac_f32_e32 v17, v20, v164
	v_fmac_f32_e32 v17, v21, v165
	ds_read_b128 v[18:21], v3 offset:37648
	s_waitcnt lgkmcnt(0)
	v_fmac_f32_e32 v17, v18, v156
	v_fmac_f32_e32 v17, v19, v157
	v_fmac_f32_e32 v17, v20, v160
	v_fmac_f32_e32 v17, v21, v161
	ds_read_b128 v[18:21], v3 offset:37664
	s_waitcnt lgkmcnt(0)
	v_fmac_f32_e32 v17, v18, v154
	v_fmac_f32_e32 v17, v19, v155
	v_fmac_f32_e32 v17, v20, v158
	v_fmac_f32_e32 v17, v21, v159
	ds_read_b128 v[18:21], v3 offset:37680
	s_waitcnt lgkmcnt(0)
	v_fmac_f32_e32 v17, v18, v151
	v_fmac_f32_e32 v17, v19, v150
	v_fmac_f32_e32 v17, v20, v153
	v_fmac_f32_e32 v17, v21, v152
	v_min_f32_e32 v18, 0, v17
	v_mul_f32_e64 v17, |v17|, s20
	v_exp_f32_e32 v17, v17
	s_nop 0
	v_add_f32_e32 v17, 1.0, v17
	v_cmp_gt_f32_e32 vcc, s21, v17
	s_nop 1
	v_cndmask_b32_e64 v19, 0, 32, vcc
	v_ldexp_f32 v17, v17, v19
	v_log_f32_e32 v17, v17
	s_nop 0
	v_mul_f32_e32 v19, 0x3f317217, v17
	v_fma_f32 v19, v17, s22, -v19
	v_fmac_f32_e32 v19, 0x3377d1cf, v17
	v_fmac_f32_e32 v19, 0x3f317217, v17
	v_cmp_lt_f32_e64 s[74:75], |v17|, s23
	s_nop 1
	v_cndmask_b32_e64 v17, v17, v19, s[74:75]
	v_cndmask_b32_e32 v19, 0, v145, vcc
	v_sub_f32_e32 v17, v17, v19
	v_sub_f32_e32 v17, v18, v17
	ds_read_b128 v[18:21], v3 offset:37696
	v_fmamk_f32 v17, v17, 0x3d800000, v16
	s_waitcnt lgkmcnt(0)
	v_fma_f32 v22, v18, v162, v149
	v_fmac_f32_e32 v22, v19, v163
	v_fmac_f32_e32 v22, v20, v164
	v_fmac_f32_e32 v22, v21, v165
	ds_read_b128 v[18:21], v3 offset:37712
	s_waitcnt lgkmcnt(0)
	v_fmac_f32_e32 v22, v18, v156
	v_fmac_f32_e32 v22, v19, v157
	v_fmac_f32_e32 v22, v20, v160
	v_fmac_f32_e32 v22, v21, v161
	ds_read_b128 v[18:21], v3 offset:37728
	s_waitcnt lgkmcnt(0)
	v_fmac_f32_e32 v22, v18, v154
	v_fmac_f32_e32 v22, v19, v155
	v_fmac_f32_e32 v22, v20, v158
	v_fmac_f32_e32 v22, v21, v159
	ds_read_b128 v[18:21], v3 offset:37744
	s_waitcnt lgkmcnt(0)
	v_fmac_f32_e32 v22, v18, v151
	v_fmac_f32_e32 v22, v19, v150
	v_fmac_f32_e32 v22, v20, v153
	v_fmac_f32_e32 v22, v21, v152
	v_mul_f32_e64 v19, |v22|, s20
	v_exp_f32_e32 v19, v19
	v_min_f32_e32 v18, 0, v22
	v_add_f32_e32 v19, 1.0, v19
	v_cmp_gt_f32_e32 vcc, s21, v19
	s_nop 1
	v_cndmask_b32_e64 v20, 0, 32, vcc
	v_ldexp_f32 v19, v19, v20
	v_log_f32_e32 v19, v19
	s_nop 0
	v_mul_f32_e32 v20, 0x3f317217, v19
	v_fma_f32 v20, v19, s22, -v20
	v_fmac_f32_e32 v20, 0x3377d1cf, v19
	v_fmac_f32_e32 v20, 0x3f317217, v19
	v_cmp_lt_f32_e64 s[74:75], |v19|, s23
	s_nop 1
	v_cndmask_b32_e64 v19, v19, v20, s[74:75]
	v_cndmask_b32_e32 v20, 0, v145, vcc
	v_sub_f32_e32 v19, v19, v20
	ds_read_b128 v[20:23], v3 offset:37760
	v_sub_f32_e32 v18, v18, v19
	v_fmamk_f32 v18, v18, 0x3d800000, v17
	s_waitcnt lgkmcnt(0)
	v_fma_f32 v19, v20, v162, v149
	v_fmac_f32_e32 v19, v21, v163
	v_fmac_f32_e32 v19, v22, v164
	v_fmac_f32_e32 v19, v23, v165
	ds_read_b128 v[20:23], v3 offset:37776
	s_waitcnt lgkmcnt(0)
	v_fmac_f32_e32 v19, v20, v156
	v_fmac_f32_e32 v19, v21, v157
	v_fmac_f32_e32 v19, v22, v160
	v_fmac_f32_e32 v19, v23, v161
	ds_read_b128 v[20:23], v3 offset:37792
	s_waitcnt lgkmcnt(0)
	v_fmac_f32_e32 v19, v20, v154
	v_fmac_f32_e32 v19, v21, v155
	v_fmac_f32_e32 v19, v22, v158
	v_fmac_f32_e32 v19, v23, v159
	ds_read_b128 v[20:23], v3 offset:37808
	s_waitcnt lgkmcnt(0)
	v_fmac_f32_e32 v19, v20, v151
	v_fmac_f32_e32 v19, v21, v150
	v_fmac_f32_e32 v19, v22, v153
	v_fmac_f32_e32 v19, v23, v152
	v_min_f32_e32 v20, 0, v19
	v_mul_f32_e64 v19, |v19|, s20
	v_exp_f32_e32 v19, v19
	s_nop 0
	v_add_f32_e32 v19, 1.0, v19
	v_cmp_gt_f32_e32 vcc, s21, v19
	s_nop 1
	v_cndmask_b32_e64 v21, 0, 32, vcc
	v_ldexp_f32 v19, v19, v21
	v_log_f32_e32 v19, v19
	s_nop 0
	v_mul_f32_e32 v21, 0x3f317217, v19
	v_fma_f32 v21, v19, s22, -v21
	v_fmac_f32_e32 v21, 0x3377d1cf, v19
	v_fmac_f32_e32 v21, 0x3f317217, v19
	v_cmp_lt_f32_e64 s[74:75], |v19|, s23
	s_nop 1
	v_cndmask_b32_e64 v19, v19, v21, s[74:75]
	v_cndmask_b32_e32 v21, 0, v145, vcc
	v_sub_f32_e32 v19, v19, v21
	v_sub_f32_e32 v19, v20, v19
	ds_read_b128 v[20:23], v3 offset:37824
	v_fmamk_f32 v19, v19, 0x3d800000, v18
	s_waitcnt lgkmcnt(0)
	v_fmac_f32_e32 v149, v20, v162
	v_fmac_f32_e32 v149, v21, v163
	v_fmac_f32_e32 v149, v22, v164
	v_fmac_f32_e32 v149, v23, v165
	ds_read_b128 v[20:23], v3 offset:37840
	s_waitcnt lgkmcnt(0)
	v_fmac_f32_e32 v149, v20, v156
	v_fmac_f32_e32 v149, v21, v157
	v_fmac_f32_e32 v149, v22, v160
	v_fmac_f32_e32 v149, v23, v161
	ds_read_b128 v[20:23], v3 offset:37856
	s_waitcnt lgkmcnt(0)
	v_fmac_f32_e32 v149, v20, v154
	v_fmac_f32_e32 v149, v21, v155
	v_fmac_f32_e32 v149, v22, v158
	v_fmac_f32_e32 v149, v23, v159
	ds_read_b128 v[20:23], v3 offset:37872
	s_waitcnt lgkmcnt(0)
	v_fmac_f32_e32 v149, v20, v151
	v_fmac_f32_e32 v149, v21, v150
	v_fmac_f32_e32 v149, v22, v153
	v_fmac_f32_e32 v149, v23, v152
	v_mul_f32_e64 v20, |v149|, s20
	v_exp_f32_e32 v20, v20
	v_min_f32_e32 v3, 0, v149
	v_add_f32_e32 v20, 1.0, v20
	v_cmp_gt_f32_e32 vcc, s21, v20
	s_nop 1
	v_cndmask_b32_e64 v21, 0, 32, vcc
	v_ldexp_f32 v20, v20, v21
	v_log_f32_e32 v20, v20
	s_nop 0
	v_mul_f32_e32 v21, 0x3f317217, v20
	v_fma_f32 v21, v20, s22, -v21
	v_fmac_f32_e32 v21, 0x3377d1cf, v20
	v_fmac_f32_e32 v21, 0x3f317217, v20
	v_cmp_lt_f32_e64 s[74:75], |v20|, s23
	s_nop 1
	v_cndmask_b32_e64 v20, v20, v21, s[74:75]
	v_cndmask_b32_e32 v21, 0, v145, vcc
	v_sub_f32_e32 v20, v20, v21
	v_sub_f32_e32 v3, v3, v20
	v_fmamk_f32 v20, v3, 0x3d800000, v19
	v_lshl_add_u32 v3, v2, 2, 0
	v_cmp_lt_u32_e32 vcc, s2, v2
	v_mov_b32_e32 v21, 0
	ds_write_b32 v3, v20 offset:34816
	s_waitcnt lgkmcnt(0)
	s_barrier
	s_and_saveexec_b64 s[2:3], vcc
	s_cbranch_execz .LBB0_998
	v_and_b32_e32 v2, 0x7f, v2
	v_lshl_add_u32 v21, v2, 2, 0
	ds_read2st64_b32 v[2:3], v21 offset0:136 offset1:138
	ds_read_b32 v22, v21 offset:35840
	v_cmp_lt_i32_e32 vcc, 1, v4
	s_mov_b64 s[8:9], 0
	s_and_saveexec_b64 s[10:11], vcc
	s_xor_b64 s[10:11], exec, s[10:11]
	s_cbranch_execnz .LBB0_1030
	s_andn2_saveexec_b64 s[10:11], s[10:11]
	s_cbranch_execnz .LBB0_1033
